# P0 weight-conversion loop software-pipelined: next item's tile + int8 column scales loaded by a generic address generator at loop head while current item converts
# baseline (speedup 1.0000x reference)
.LBB0_85:
	s_or_b64 exec, exec, s[0:1]
	s_cmp_gt_i32 s6, 0x28bff
	v_lshlrev_b32_e32 v92, 3, v1
	s_waitcnt lgkmcnt(0)
	s_barrier
	s_cbranch_scc1 .LBB0_136
	s_lshl_b32 s0, s3, 8
	s_and_b32 s0, s0, 0x7fffc000
	v_lshrrev_b32_e32 v35, 3, v1
	v_and_b32_e32 v24, 28, v34
	s_add_i32 s0, s0, 0
	v_mul_u32_u24_e32 v2, 0x84, v35
	v_lshlrev_b32_e32 v4, 2, v24
	v_add3_u32 v62, s0, v2, v4
	v_and_b32_e32 v2, 48, v90
	v_and_b32_e32 v10, 56, v92
	v_mul_u32_u24_e32 v6, 0x84, v2
	v_and_b32_e32 v7, 60, v1
	v_mul_u32_u24_e32 v12, 0x84, v10
	v_lshlrev_b32_e32 v13, 2, v35
	v_mov_b32_e32 v3, 0
	v_readlane_b32 s12, v247, 61
	v_add3_u32 v64, s0, v6, v7
	v_add3_u32 v66, s0, v12, v13
	v_readlane_b32 s0, v247, 57
	v_readlane_b32 s13, v247, 62
	v_lshlrev_b32_e32 v14, 1, v10
	v_mov_b32_e32 v15, v3
	v_readlane_b32 s1, v247, 58
	v_lshl_add_u64 v[4:5], s[12:13], 0, v[2:3]
	v_readlane_b32 s12, v246, 1
	v_lshl_add_u64 v[10:11], s[76:77], 0, v[14:15]
	v_lshl_add_u64 v[12:13], s[0:1], 0, v[2:3]
	v_lshl_add_u64 v[14:15], s[86:87], 0, v[14:15]
	s_mov_b64 s[0:1], 0x54600000
	v_readlane_b32 s13, v246, 2
	v_lshl_add_u64 v[14:15], v[14:15], 0, s[0:1]
	v_readlane_b32 s0, v247, 63
	v_lshl_add_u64 v[6:7], s[12:13], 0, v[2:3]
	v_readlane_b32 s12, v247, 59
	v_readlane_b32 s1, v246, 0
	v_lshrrev_b32_e32 v63, 2, v1
	v_readlane_b32 s13, v247, 60
	v_lshl_add_u64 v[16:17], s[0:1], 0, v[2:3]
	s_lshl_b32 s0, s6, 2
	s_mov_b32 s11, 0
	v_or_b32_e32 v65, 16, v63
	v_lshl_add_u64 v[8:9], s[12:13], 0, v[2:3]
	v_or_b32_e32 v67, 8, v35
	v_or_b32_e32 v68, 16, v35
	v_or_b32_e32 v69, 24, v35
	v_lshl_add_u64 v[18:19], s[8:9], 0, v[2:3]
	v_lshl_add_u64 v[20:21], s[84:85], 0, v[2:3]
	v_lshl_add_u64 v[22:23], s[26:27], 0, v[2:3]
	s_lshl_b32 s14, s6, 5
	s_lshl_b32 s15, s92, 5
	s_add_i32 s16, s0, 0x1f800
	s_lshl_b32 s17, s92, 2
	s_mov_b32 s18, 0x20000
	s_mov_b32 s19, 0x40000
	s_mov_b32 s20, 0x60000
	s_mov_b32 s21, 0x80000
	s_mov_b32 s30, 0xa0000
	s_mov_b32 s31, 0xc0000
	s_mov_b32 s34, 0xe0000
	v_add_u32_e32 v70, 0x420, v62
	v_add_u32_e32 v71, 0x428, v62
	v_add_u32_e32 v72, 0x840, v62
	v_add_u32_e32 v73, 0x848, v62
	v_add_u32_e32 v74, 0xc60, v62
	v_add_u32_e32 v75, 0xc68, v62
	v_add_u32_e32 v76, 0x1080, v62
	v_add_u32_e32 v77, 0x1088, v62
	v_add_u32_e32 v78, 0x14a0, v62
	v_add_u32_e32 v79, 0x14a8, v62
	v_add_u32_e32 v80, 0x18c0, v62
	v_add_u32_e32 v81, 0x18c8, v62
	v_add_u32_e32 v82, 0x1ce0, v62
	v_add_u32_e32 v83, 0x1ce8, v62
	s_mov_b32 s35, 0xc3e00000
	s_mov_b32 s52, 0x60005
	s_mov_b32 s53, 0x56000
	s_mov_b32 s54, 0xac000
	s_mov_b32 s55, 0x102000
	s_mov_b32 s56, 0x158000
	s_mov_b32 s57, 0x1ae000
	s_mov_b32 s58, 0x204000
	s_mov_b32 s59, 0x25a000
	s_movk_i32 s72, 0x4000
	s_mov_b32 s73, 0x8000
	s_mov_b32 s74, 0xc000
	s_mov_b32 s75, 0x10000
	s_mov_b32 s64, 0x14000
	s_mov_b32 s65, 0x18000
	s_mov_b32 s66, 0x1c000
	s_movk_i32 s67, 0x7fff
	s_mov_b32 s68, 0xffff0000
	s_mov_b32 s69, 0x48000
	s_mov_b32 s70, 0x90000
	s_mov_b32 s71, 0xd8000
	s_mov_b32 s93, 0x120000
	s_mov_b32 s94, 0x168000
	s_mov_b32 s95, 0x1b0000
	s_mov_b32 s60, 0x1f8000
	s_mov_b32 s61, 0x42fe0000
	s_mov_b32 s62, 0xc2fe0000
	s_mov_b32 s63, 0xc0c0500
	v_lshlrev_b32_e32 v2, 2, v24
	v_mov_b32_e32 v84, 0x43e00000
	v_add_u32_e32 v85, 0x400, v64
	v_mov_b32_e32 v86, 0x42fe0000
	s_mov_b32 s3, s6
	v_writelane_b32 v254, s76, 0
	v_writelane_b32 v254, s77, 1
	v_writelane_b32 v254, s78, 2
	v_writelane_b32 v254, s79, 3
	v_writelane_b32 v254, s80, 4
	v_writelane_b32 v254, s81, 5
	v_writelane_b32 v254, s82, 6
	v_writelane_b32 v254, s83, 7
	s_mov_b32 s98, s3
	v_readlane_b32 s100, v246, 3
	v_readlane_b32 s101, v246, 4
	s_mov_b32 s76, 0
	s_mov_b32 s77, 16
	s_mov_b32 s78, 0x158
	s_mov_b32 s79, 0xbe83
	s_mov_b32 s80, 0
	s_mov_b32 s81, 0x158
	s_mov_b64 s[82:83], s[28:29]
	s_cmp_ge_u32 s98, 0x5600
	s_cselect_b32 s76, 0x5600, s76
	s_cselect_b32 s77, 18, s77
	s_cselect_b64 s[82:83], s[4:5], s[82:83]
	s_cmp_ge_u32 s98, 0xac00
	s_cselect_b32 s76, 0xac00, s76
	s_cselect_b32 s77, 20, s77
	s_cselect_b32 s78, 0x80, s78
	s_cselect_b32 s79, 0x20000, s79
	s_cselect_b32 s81, 0x80, s81
	s_cmp_ge_u32 s98, 0x10200
	s_cselect_b32 s76, 0x10200, s76
	s_cselect_b32 s77, 24, s77
	s_cselect_b32 s78, 0x120, s78
	s_cselect_b32 s79, 0xe38f, s79
	s_cselect_b32 s81, 0x120, s81
	s_cselect_b64 s[82:83], s[90:91], s[82:83]
	s_cmp_ge_u32 s98, 0x14a00
	s_cselect_b32 s76, 0x14a00, s76
	s_cselect_b32 s77, 34, s77
	s_cselect_b32 s78, 0x80, s78
	s_cselect_b32 s79, 0x20000, s79
	s_cselect_b32 s81, 0x80, s81
	s_cselect_b64 s[82:83], s[100:101], s[82:83]
	s_cmp_ge_u32 s98, 0x16a00
	s_cselect_b32 s76, 0x16a00, s76
	s_cselect_b32 s77, 24, s77
	s_cselect_b32 s78, 64, s78
	s_cselect_b32 s79, 0x40000, s79
	s_cselect_b32 s80, 64, s80
	s_cselect_b32 s81, 0x120, s81
	s_cmp_ge_u32 s98, 0x17a00
	s_cselect_b32 s76, 0x17a00, s76
	s_cselect_b32 s77, 43, s77
	s_cselect_b32 s78, 16, s78
	s_cselect_b32 s79, 0x100000, s79
	s_cselect_b32 s80, 0, s80
	s_cselect_b32 s81, 16, s81
	s_cmp_ge_u32 s98, 0x17e00
	s_cselect_b32 s76, 0x17e00, s76
	s_cselect_b32 s77, 45, s77
	s_cmp_ge_u32 s98, 0x18200
	s_cselect_b32 s76, 0x18200, s76
	s_cselect_b32 s77, 47, s77
	s_cmp_ge_u32 s98, 0x18600
	s_cselect_b32 s76, 0x18600, s76
	s_cselect_b32 s77, 49, s77
	s_cselect_b32 s78, 0x80, s78
	s_cselect_b32 s79, 0x20000, s79
	s_cselect_b32 s81, 0x80, s81
	s_cmp_ge_u32 s98, 0x18a00
	s_cselect_b32 s76, 0x18a00, s76
	s_cselect_b32 s77, 53, s77
	s_cselect_b32 s78, 0x158, s78
	s_cselect_b32 s79, 0xbe83, s79
	s_cselect_b32 s81, 0x158, s81
	s_cmp_ge_u32 s98, 0x1e000
	s_cselect_b32 s76, 0x1e000, s76
	s_cselect_b32 s77, 55, s77
	s_cmp_ge_u32 s98, 0x23600
	s_cselect_b32 s76, 0x23600, s76
	s_cselect_b32 s77, 2, s77
	s_cselect_b32 s78, 0x80, s78
	s_cselect_b32 s79, 0x20000, s79
	s_cselect_b32 s81, 0x80, s81
	s_sub_u32 s98, s98, s76
	s_mul_i32 s99, s98, s79
	s_lshr_b32 s99, s99, 24
	s_mul_i32 s76, s99, s78
	s_sub_u32 s98, s98, s76
	s_lshl_b32 s79, s98, 7
	s_add_u32 s98, s98, s80
	s_lshl_b32 s98, s98, 7
	s_mul_i32 s99, s99, s81
	s_lshl_b32 s99, s99, 13
	s_add_u32 s98, s98, s99
	s_add_i32 s78, s77, 1
	s_lshl_b32 s81, s81, 7
	s_nop 3
	v_readlane_b32 s100, v247, s77
	v_readlane_b32 s101, v247, s78
	v_mad_u32_u24 v252, v35, s81, v2
	v_lshl_add_u32 v251, v63, 2, s79
	s_lshl_b32 s81, s81, 3
	s_add_u32 s100, s100, s98
	s_addc_u32 s101, s101, 0
	global_load_dword v232, v251, s[82:83]
	global_load_dword v233, v251, s[82:83] offset:64
	global_load_dwordx4 v[200:203], v252, s[100:101]
	s_add_u32 s100, s100, s81
	s_addc_u32 s101, s101, 0
	global_load_dwordx4 v[204:207], v252, s[100:101]
	s_add_u32 s100, s100, s81
	s_addc_u32 s101, s101, 0
	global_load_dwordx4 v[208:211], v252, s[100:101]
	s_add_u32 s100, s100, s81
	s_addc_u32 s101, s101, 0
	global_load_dwordx4 v[212:215], v252, s[100:101]
	s_add_u32 s100, s100, s81
	s_addc_u32 s101, s101, 0
	global_load_dwordx4 v[216:219], v252, s[100:101]
	s_add_u32 s100, s100, s81
	s_addc_u32 s101, s101, 0
	global_load_dwordx4 v[220:223], v252, s[100:101]
	s_add_u32 s100, s100, s81
	s_addc_u32 s101, s101, 0
	global_load_dwordx4 v[224:227], v252, s[100:101]
	s_add_u32 s100, s100, s81
	s_addc_u32 s101, s101, 0
	global_load_dwordx4 v[228:231], v252, s[100:101]
	s_waitcnt vmcnt(0)
	s_branch .Lp0_body
.Lp0_exit:
	s_waitcnt vmcnt(0)
	v_readlane_b32 s76, v254, 0
	v_readlane_b32 s77, v254, 1
	v_readlane_b32 s78, v254, 2
	v_readlane_b32 s79, v254, 3
	v_readlane_b32 s80, v254, 4
	v_readlane_b32 s81, v254, 5
	v_readlane_b32 s82, v254, 6
	v_readlane_b32 s83, v254, 7
	s_branch .LBB0_136

.LBB0_88:
	s_waitcnt vmcnt(2)
.Lp0_body:
	ds_write2_b32 v62, v200, v201 offset1:1
	ds_write2_b32 v62, v202, v203 offset0:2 offset1:3
	ds_write2_b32 v70, v204, v205 offset1:1
	ds_write2_b32 v71, v206, v207 offset1:1
	ds_write2_b32 v72, v208, v209 offset1:1
	ds_write2_b32 v73, v210, v211 offset1:1
	ds_write2_b32 v74, v212, v213 offset1:1
	ds_write2_b32 v75, v214, v215 offset1:1
	ds_write2_b32 v76, v216, v217 offset1:1
	ds_write2_b32 v77, v218, v219 offset1:1
	ds_write2_b32 v78, v220, v221 offset1:1
	ds_write2_b32 v79, v222, v223 offset1:1
	ds_write2_b32 v80, v224, v225 offset1:1
	ds_write2_b32 v81, v226, v227 offset1:1
	ds_write2_b32 v82, v228, v229 offset1:1
	ds_write2_b32 v83, v230, v231 offset1:1
	v_mov_b32_e32 v234, v232
	v_mov_b32_e32 v235, v233
	s_add_i32 s98, s3, s92
	s_cmp_gt_i32 s98, 0x28bff
	s_cselect_b32 s98, s3, s98
	v_readlane_b32 s100, v246, 3
	v_readlane_b32 s101, v246, 4
	s_mov_b32 s76, 0
	s_mov_b32 s77, 16
	s_mov_b32 s78, 0x158
	s_mov_b32 s79, 0xbe83
	s_mov_b32 s80, 0
	s_mov_b32 s81, 0x158
	s_mov_b64 s[82:83], s[28:29]
	s_cmp_ge_u32 s98, 0x5600
	s_cselect_b32 s76, 0x5600, s76
	s_cselect_b32 s77, 18, s77
	s_cselect_b64 s[82:83], s[4:5], s[82:83]
	s_cmp_ge_u32 s98, 0xac00
	s_cselect_b32 s76, 0xac00, s76
	s_cselect_b32 s77, 20, s77
	s_cselect_b32 s78, 0x80, s78
	s_cselect_b32 s79, 0x20000, s79
	s_cselect_b32 s81, 0x80, s81
	s_cmp_ge_u32 s98, 0x10200
	s_cselect_b32 s76, 0x10200, s76
	s_cselect_b32 s77, 24, s77
	s_cselect_b32 s78, 0x120, s78
	s_cselect_b32 s79, 0xe38f, s79
	s_cselect_b32 s81, 0x120, s81
	s_cselect_b64 s[82:83], s[90:91], s[82:83]
	s_cmp_ge_u32 s98, 0x14a00
	s_cselect_b32 s76, 0x14a00, s76
	s_cselect_b32 s77, 34, s77
	s_cselect_b32 s78, 0x80, s78
	s_cselect_b32 s79, 0x20000, s79
	s_cselect_b32 s81, 0x80, s81
	s_cselect_b64 s[82:83], s[100:101], s[82:83]
	s_cmp_ge_u32 s98, 0x16a00
	s_cselect_b32 s76, 0x16a00, s76
	s_cselect_b32 s77, 24, s77
	s_cselect_b32 s78, 64, s78
	s_cselect_b32 s79, 0x40000, s79
	s_cselect_b32 s80, 64, s80
	s_cselect_b32 s81, 0x120, s81
	s_cmp_ge_u32 s98, 0x17a00
	s_cselect_b32 s76, 0x17a00, s76
	s_cselect_b32 s77, 43, s77
	s_cselect_b32 s78, 16, s78
	s_cselect_b32 s79, 0x100000, s79
	s_cselect_b32 s80, 0, s80
	s_cselect_b32 s81, 16, s81
	s_cmp_ge_u32 s98, 0x17e00
	s_cselect_b32 s76, 0x17e00, s76
	s_cselect_b32 s77, 45, s77
	s_cmp_ge_u32 s98, 0x18200
	s_cselect_b32 s76, 0x18200, s76
	s_cselect_b32 s77, 47, s77
	s_cmp_ge_u32 s98, 0x18600
	s_cselect_b32 s76, 0x18600, s76
	s_cselect_b32 s77, 49, s77
	s_cselect_b32 s78, 0x80, s78
	s_cselect_b32 s79, 0x20000, s79
	s_cselect_b32 s81, 0x80, s81
	s_cmp_ge_u32 s98, 0x18a00
	s_cselect_b32 s76, 0x18a00, s76
	s_cselect_b32 s77, 53, s77
	s_cselect_b32 s78, 0x158, s78
	s_cselect_b32 s79, 0xbe83, s79
	s_cselect_b32 s81, 0x158, s81
	s_cmp_ge_u32 s98, 0x1e000
	s_cselect_b32 s76, 0x1e000, s76
	s_cselect_b32 s77, 55, s77
	s_cmp_ge_u32 s98, 0x23600
	s_cselect_b32 s76, 0x23600, s76
	s_cselect_b32 s77, 2, s77
	s_cselect_b32 s78, 0x80, s78
	s_cselect_b32 s79, 0x20000, s79
	s_cselect_b32 s81, 0x80, s81
	s_sub_u32 s98, s98, s76
	s_mul_i32 s99, s98, s79
	s_lshr_b32 s99, s99, 24
	s_mul_i32 s76, s99, s78
	s_sub_u32 s98, s98, s76
	s_lshl_b32 s79, s98, 7
	s_add_u32 s98, s98, s80
	s_lshl_b32 s98, s98, 7
	s_mul_i32 s99, s99, s81
	s_lshl_b32 s99, s99, 13
	s_add_u32 s98, s98, s99
	s_add_i32 s78, s77, 1
	s_lshl_b32 s81, s81, 7
	s_nop 3
	v_readlane_b32 s100, v247, s77
	v_readlane_b32 s101, v247, s78
	v_mad_u32_u24 v252, v35, s81, v2
	v_lshl_add_u32 v251, v63, 2, s79
	s_lshl_b32 s81, s81, 3
	s_add_u32 s100, s100, s98
	s_addc_u32 s101, s101, 0
	global_load_dword v232, v251, s[82:83]
	global_load_dword v233, v251, s[82:83] offset:64
	global_load_dwordx4 v[200:203], v252, s[100:101]
	s_add_u32 s100, s100, s81
	s_addc_u32 s101, s101, 0
	global_load_dwordx4 v[204:207], v252, s[100:101]
	s_add_u32 s100, s100, s81
	s_addc_u32 s101, s101, 0
	global_load_dwordx4 v[208:211], v252, s[100:101]
	s_add_u32 s100, s100, s81
	s_addc_u32 s101, s101, 0
	global_load_dwordx4 v[212:215], v252, s[100:101]
	s_add_u32 s100, s100, s81
	s_addc_u32 s101, s101, 0
	global_load_dwordx4 v[216:219], v252, s[100:101]
	s_add_u32 s100, s100, s81
	s_addc_u32 s101, s101, 0
	global_load_dwordx4 v[220:223], v252, s[100:101]
	s_add_u32 s100, s100, s81
	s_addc_u32 s101, s101, 0
	global_load_dwordx4 v[224:227], v252, s[100:101]
	s_add_u32 s100, s100, s81
	s_addc_u32 s101, s101, 0
	global_load_dwordx4 v[228:231], v252, s[100:101]
	s_cmpk_gt_i32 s3, 0x55ff
	s_mov_b64 s[0:1], -1
	s_cbranch_scc0 .LBB0_134
	s_cmpk_gt_u32 s3, 0xabff
	s_cbranch_scc0 .LBB0_131
	s_cmp_gt_u32 s3, 0x101ff
	s_cbranch_scc0 .LBB0_128
	s_cmp_gt_u32 s3, 0x149ff
	s_cbranch_scc0 .LBB0_125
	s_cmp_gt_u32 s3, 0x169ff
	s_cbranch_scc0 .LBB0_122
	s_cmp_gt_u32 s3, 0x179ff
	s_cbranch_scc0 .LBB0_119
	s_cmp_gt_u32 s3, 0x17dff
	s_cbranch_scc0 .LBB0_116
	s_cmp_gt_u32 s3, 0x181ff
	s_cbranch_scc0 .LBB0_113
	s_cmp_gt_u32 s3, 0x185ff
	s_cbranch_scc0 .LBB0_110
	s_cmp_gt_u32 s3, 0x189ff
	s_cbranch_scc0 .LBB0_107
	s_cmp_gt_u32 s3, 0x1dfff
	s_cbranch_scc0 .LBB0_104
	s_cmp_gt_u32 s3, 0x235ff
	s_cbranch_scc0 .LBB0_101
	s_add_i32 s0, s3, 0xca00
	s_lshr_b32 s0, s0, 1
	s_and_b32 s0, s0, 0x7fc0
	s_lshl_b32 s1, s3, 5
	v_or_b32_e32 v24, s0, v35
	v_readlane_b32 s36, v247, 2
	s_and_b32 s7, s1, 0xfe0
	v_lshlrev_b32_e32 v24, 14, v24
	v_mov_b32_e32 v25, v3
	v_readlane_b32 s37, v247, 3
	s_lshl_b32 s10, s7, 2
	v_mov_b32_e32 v94, v3
	v_lshl_add_u64 v[24:25], s[36:37], 0, v[24:25]
	v_lshl_add_u64 v[24:25], v[24:25], 0, s[10:11]
	v_lshl_add_u64 v[32:33], v[24:25], 0, v[2:3]
	v_add_co_u32_e32 v28, vcc, s18, v32
	v_mov_b32_e32 v95, v3
	s_nop 0
	v_addc_co_u32_e32 v29, vcc, 0, v33, vcc
	v_add_co_u32_e32 v36, vcc, s19, v32
	s_nop 0
	v_addc_co_u32_e32 v37, vcc, 0, v33, vcc
	v_add_co_u32_e32 v40, vcc, s20, v32
	v_mov_b32_e32 v96, v3
	s_nop 0
	v_addc_co_u32_e32 v41, vcc, 0, v33, vcc
	v_add_co_u32_e32 v44, vcc, s21, v32
	s_nop 0
	v_addc_co_u32_e32 v45, vcc, 0, v33, vcc
	v_add_co_u32_e32 v48, vcc, s30, v32
	v_mov_b32_e32 v97, v3
	s_nop 0
	v_addc_co_u32_e32 v49, vcc, 0, v33, vcc
	s_nop 0
	v_add_co_u32_e32 v52, vcc, s31, v32
	s_mov_b32 s1, s11
	s_nop 0
	v_addc_co_u32_e32 v53, vcc, 0, v33, vcc
	v_add_co_u32_e32 v32, vcc, s34, v32
	v_mov_b32_e32 v61, v3
	s_nop 0
	v_addc_co_u32_e32 v33, vcc, 0, v33, vcc
	v_lshl_add_u64 v[32:33], v[4:5], 0, s[0:1]
	v_readlane_b32 s38, v247, 4
	v_readlane_b32 s39, v247, 5
	s_mov_b64 s[0:1], 0
	s_waitcnt lgkmcnt(0)
	ds_read2_b32 v[24:25], v64 offset1:16
	ds_read2_b32 v[26:27], v64 offset0:33 offset1:49
	ds_read2_b32 v[28:29], v64 offset0:66 offset1:82
	ds_read2_b32 v[30:31], v64 offset0:99 offset1:115
	ds_read2_b32 v[36:37], v64 offset0:132 offset1:148
	ds_read2_b32 v[38:39], v64 offset0:165 offset1:181
	ds_read2_b32 v[40:41], v64 offset0:198 offset1:214
	ds_read2_b32 v[42:43], v64 offset0:231 offset1:247
	ds_read2_b32 v[44:45], v85 offset0:8 offset1:24
	ds_read2_b32 v[46:47], v85 offset0:41 offset1:57
	ds_read2_b32 v[48:49], v85 offset0:74 offset1:90
	ds_read2_b32 v[50:51], v85 offset0:107 offset1:123
	s_waitcnt lgkmcnt(11)
	v_mul_f32_e32 v24, 0x43000000, v24
	s_waitcnt lgkmcnt(10)
	v_mul_f32_e32 v26, 0x43000000, v26
	s_waitcnt lgkmcnt(7)
	v_mul_f32_e32 v36, 0x43000000, v36
	s_waitcnt lgkmcnt(6)
	v_mul_f32_e32 v38, 0x43000000, v38
	v_med3_f32 v24, v24, s35, v84
	v_med3_f32 v26, v26, s35, v84
	v_med3_f32 v36, v36, s35, v84
	v_med3_f32 v38, v38, s35, v84
	v_cvt_pk_fp8_f32 v94, v24, v26
	v_cvt_pk_fp8_f32 v95, v36, v38
	v_mul_f32_e32 v28, 0x43000000, v28
	v_mul_f32_e32 v30, 0x43000000, v30
	s_waitcnt lgkmcnt(5)
	v_mul_f32_e32 v40, 0x43000000, v40
	s_waitcnt lgkmcnt(4)
	v_mul_f32_e32 v42, 0x43000000, v42
	s_waitcnt lgkmcnt(3)
	v_mul_f32_e32 v44, 0x43000000, v44
	s_waitcnt lgkmcnt(2)
	v_mul_f32_e32 v46, 0x43000000, v46
	v_med3_f32 v28, v28, s35, v84
	v_med3_f32 v30, v30, s35, v84
	v_med3_f32 v24, v40, s35, v84
	v_med3_f32 v26, v42, s35, v84
	v_cvt_pk_fp8_f32 v94, v28, v30 op_sel:[0,0,1]
	v_cvt_pk_fp8_f32 v95, v24, v26 op_sel:[0,0,1]
	v_med3_f32 v26, v44, s35, v84
	v_med3_f32 v28, v46, s35, v84
	v_cvt_pk_fp8_f32 v96, v26, v28
	ds_read2_b32 v[52:53], v85 offset0:140 offset1:156
	ds_read2_b32 v[54:55], v85 offset0:173 offset1:189
	ds_read2_b32 v[56:57], v85 offset0:206 offset1:222
	s_waitcnt lgkmcnt(4)
	v_mul_f32_e32 v48, 0x43000000, v48
	s_waitcnt lgkmcnt(3)
	v_mul_f32_e32 v24, 0x43000000, v50
	v_med3_f32 v26, v48, s35, v84
	v_med3_f32 v24, v24, s35, v84
	ds_read2_b32 v[58:59], v85 offset0:239 offset1:255
	v_cvt_pk_fp8_f32 v96, v26, v24 op_sel:[0,0,1]
	s_waitcnt lgkmcnt(3)
	v_mul_f32_e32 v24, 0x43000000, v52
	s_waitcnt lgkmcnt(2)
	v_mul_f32_e32 v26, 0x43000000, v54
	v_med3_f32 v24, v24, s35, v84
	v_med3_f32 v26, v26, s35, v84
	v_cvt_pk_fp8_f32 v97, v24, v26
	s_waitcnt lgkmcnt(1)
	v_mul_f32_e32 v28, 0x43000000, v56
	s_waitcnt lgkmcnt(0)
	v_mul_f32_e32 v24, 0x43000000, v58
	v_med3_f32 v26, v28, s35, v84
	v_med3_f32 v24, v24, s35, v84
	v_cvt_pk_fp8_f32 v97, v26, v24 op_sel:[0,0,1]
	v_or_b32_e32 v24, s7, v63
	v_mul_u32_u24_e32 v60, 0x2b00, v24
	v_mul_f32_e32 v24, 0x43000000, v25
	v_mul_f32_e32 v25, 0x43000000, v27
	v_med3_f32 v27, v24, s35, v84
	v_med3_f32 v25, v25, s35, v84
	v_mov_b32_e32 v24, v3
	v_cvt_pk_fp8_f32 v24, v27, v25
	v_mul_f32_e32 v26, 0x43000000, v29
	v_mul_f32_e32 v25, 0x43000000, v31
	v_med3_f32 v26, v26, s35, v84
	v_med3_f32 v25, v25, s35, v84
	v_cvt_pk_fp8_f32 v24, v26, v25 op_sel:[0,0,1]
	v_mul_f32_e32 v25, 0x43000000, v37
	v_mul_f32_e32 v26, 0x43000000, v39
	v_med3_f32 v28, v25, s35, v84
	v_med3_f32 v26, v26, s35, v84
	v_mov_b32_e32 v25, v3
	v_cvt_pk_fp8_f32 v25, v28, v26
	v_mul_f32_e32 v27, 0x43000000, v41
	v_mul_f32_e32 v26, 0x43000000, v43
	v_med3_f32 v27, v27, s35, v84
	v_med3_f32 v26, v26, s35, v84
	v_cvt_pk_fp8_f32 v25, v27, v26 op_sel:[0,0,1]
	v_mul_f32_e32 v26, 0x43000000, v45
	v_mul_f32_e32 v27, 0x43000000, v47
	v_med3_f32 v29, v26, s35, v84
	v_med3_f32 v27, v27, s35, v84
	v_mov_b32_e32 v26, v3
	v_cvt_pk_fp8_f32 v26, v29, v27
	v_mul_f32_e32 v28, 0x43000000, v49
	v_mul_f32_e32 v27, 0x43000000, v51
	v_med3_f32 v28, v28, s35, v84
	v_med3_f32 v27, v27, s35, v84
	v_cvt_pk_fp8_f32 v26, v28, v27 op_sel:[0,0,1]
	v_mul_f32_e32 v27, 0x43000000, v53
	v_mul_f32_e32 v28, 0x43000000, v55
	v_med3_f32 v30, v27, s35, v84
	v_med3_f32 v28, v28, s35, v84
	v_mov_b32_e32 v27, v3
	v_cvt_pk_fp8_f32 v27, v30, v28
	v_mul_f32_e32 v29, 0x43000000, v57
	v_mul_f32_e32 v28, 0x43000000, v59
	v_med3_f32 v29, v29, s35, v84
	v_med3_f32 v28, v28, s35, v84
	v_cvt_pk_fp8_f32 v27, v29, v28 op_sel:[0,0,1]
	v_or_b32_e32 v28, s7, v65
	v_mul_u32_u24_e32 v28, 0x2b00, v28
	v_mov_b32_e32 v29, v3
	v_lshl_add_u64 v[60:61], v[32:33], 0, v[60:61]
	v_lshl_add_u64 v[28:29], v[32:33], 0, v[28:29]
	global_store_dwordx4 v[60:61], v[94:97], off
	global_store_dwordx4 v[28:29], v[24:27], off
	s_waitcnt lgkmcnt(0)
.LBB0_101:
	s_andn2_b64 vcc, exec, s[0:1]
	s_cbranch_vccnz .LBB0_103
	s_add_i32 s0, s3, 0x2000
	s_and_b32 s1, s0, 0xffff
	s_mul_i32 s1, s1, 0xbe83
	s_lshr_b32 s1, s1, 24
	s_mul_i32 s7, s1, 0x158
	s_sub_i32 s0, s0, s7
	s_lshl_b32 s10, s1, 6
	v_mov_b32_e32 v24, s0
	v_pk_lshlrev_b16 v60, s52, v24 op_sel_hi:[1,0]
	v_or_b32_e32 v24, s10, v35
	v_mul_u32_u24_e32 v24, 0x2b00, v24
	v_readlane_b32 s36, v247, 41
	v_lshlrev_b32_e32 v24, 2, v24
	v_mov_b32_e32 v25, v3
	v_readlane_b32 s50, v247, 55
	v_readlane_b32 s51, v247, 56
	v_and_b32_e32 v26, 0x7fe0, v60
	v_lshlrev_b32_e32 v26, 2, v26
	v_lshl_add_u64 v[24:25], s[50:51], 0, v[24:25]
	v_mov_b32_e32 v27, v3
	v_lshl_add_u64 v[24:25], v[24:25], 0, v[26:27]
	v_lshl_add_u64 v[32:33], v[24:25], 0, v[2:3]
	v_add_co_u32_e32 v28, vcc, s53, v32
	v_mov_b32_e32 v95, v3
	s_nop 0
	v_addc_co_u32_e32 v29, vcc, 0, v33, vcc
	v_add_co_u32_e32 v36, vcc, s54, v32
	s_nop 0
	v_addc_co_u32_e32 v37, vcc, 0, v33, vcc
	v_add_co_u32_e32 v40, vcc, s55, v32
	v_mov_b32_e32 v94, v3
	s_nop 0
	v_addc_co_u32_e32 v41, vcc, 0, v33, vcc
	v_add_co_u32_e32 v44, vcc, s56, v32
	s_nop 0
	v_addc_co_u32_e32 v45, vcc, 0, v33, vcc
	v_add_co_u32_e32 v48, vcc, s57, v32
	v_mov_b32_e32 v96, v3
	s_nop 0
	v_addc_co_u32_e32 v49, vcc, 0, v33, vcc
	s_nop 0
	v_add_co_u32_e32 v52, vcc, s58, v32
	v_readfirstlane_b32 s0, v60
	s_nop 0
	v_addc_co_u32_e32 v53, vcc, 0, v33, vcc
	v_add_co_u32_e32 v32, vcc, s59, v32
	s_and_b32 s0, s0, 0x7f000060
	s_nop 0
	v_addc_co_u32_e32 v33, vcc, 0, v33, vcc
	v_mov_b32_e32 v97, v3
	s_lshr_b32 s1, s0, 16
	s_or_b32 s0, s0, s1
	s_bitset1_b32 s0, 7
	s_and_b32 s0, s0, 0xffff
	v_lshl_add_u64 v[32:33], v[6:7], 0, s[10:11]
	v_mov_b32_e32 v61, v3
	v_readlane_b32 s37, v247, 42
	v_readlane_b32 s38, v247, 43
	v_readlane_b32 s39, v247, 44
	v_readlane_b32 s40, v247, 45
	v_readlane_b32 s41, v247, 46
	v_readlane_b32 s42, v247, 47
	v_readlane_b32 s43, v247, 48
	v_readlane_b32 s44, v247, 49
	v_readlane_b32 s45, v247, 50
	v_readlane_b32 s46, v247, 51
	v_readlane_b32 s47, v247, 52
	v_readlane_b32 s48, v247, 53
	v_readlane_b32 s49, v247, 54
	s_waitcnt lgkmcnt(0)
	ds_read2_b32 v[24:25], v64 offset1:16
	ds_read2_b32 v[26:27], v64 offset0:33 offset1:49
	ds_read2_b32 v[28:29], v64 offset0:66 offset1:82
	ds_read2_b32 v[30:31], v64 offset0:99 offset1:115
	ds_read2_b32 v[36:37], v64 offset0:132 offset1:148
	ds_read2_b32 v[38:39], v64 offset0:165 offset1:181
	ds_read2_b32 v[40:41], v64 offset0:198 offset1:214
	ds_read2_b32 v[42:43], v64 offset0:231 offset1:247
	s_waitcnt lgkmcnt(7)
	v_mul_f32_e32 v24, 0x42800000, v24
	s_waitcnt lgkmcnt(3)
	v_mul_f32_e32 v36, 0x42800000, v36
	s_waitcnt lgkmcnt(2)
	v_mul_f32_e32 v38, 0x42800000, v38
	v_med3_f32 v36, v36, s35, v84
	v_med3_f32 v38, v38, s35, v84
	v_cvt_pk_fp8_f32 v95, v36, v38
	v_mul_f32_e32 v26, 0x42800000, v26
	ds_read2_b32 v[44:45], v85 offset0:8 offset1:24
	ds_read2_b32 v[46:47], v85 offset0:41 offset1:57
	ds_read2_b32 v[48:49], v85 offset0:74 offset1:90
	ds_read2_b32 v[50:51], v85 offset0:107 offset1:123
	s_waitcnt lgkmcnt(5)
	v_mul_f32_e32 v40, 0x42800000, v40
	s_waitcnt lgkmcnt(4)
	v_mul_f32_e32 v42, 0x42800000, v42
	v_med3_f32 v24, v24, s35, v84
	v_med3_f32 v26, v26, s35, v84
	v_cvt_pk_fp8_f32 v94, v24, v26
	v_med3_f32 v24, v40, s35, v84
	v_med3_f32 v26, v42, s35, v84
	v_cvt_pk_fp8_f32 v95, v24, v26 op_sel:[0,0,1]
	s_waitcnt lgkmcnt(3)
	v_mul_f32_e32 v24, 0x42800000, v44
	s_waitcnt lgkmcnt(2)
	v_mul_f32_e32 v26, 0x42800000, v46
	v_med3_f32 v24, v24, s35, v84
	v_med3_f32 v26, v26, s35, v84
	v_mul_f32_e32 v28, 0x42800000, v28
	v_mul_f32_e32 v30, 0x42800000, v30
	v_cvt_pk_fp8_f32 v96, v24, v26
	ds_read2_b32 v[52:53], v85 offset0:140 offset1:156
	ds_read2_b32 v[54:55], v85 offset0:173 offset1:189
	ds_read2_b32 v[56:57], v85 offset0:206 offset1:222
	v_med3_f32 v28, v28, s35, v84
	v_med3_f32 v30, v30, s35, v84
	v_cvt_pk_fp8_f32 v94, v28, v30 op_sel:[0,0,1]
	s_waitcnt lgkmcnt(4)
	v_mul_f32_e32 v28, 0x42800000, v48
	s_waitcnt lgkmcnt(3)
	v_mul_f32_e32 v30, 0x42800000, v50
	v_med3_f32 v24, v28, s35, v84
	v_med3_f32 v26, v30, s35, v84
	ds_read2_b32 v[58:59], v85 offset0:239 offset1:255
	v_cvt_pk_fp8_f32 v96, v24, v26 op_sel:[0,0,1]
	s_waitcnt lgkmcnt(3)
	v_mul_f32_e32 v24, 0x42800000, v52
	s_waitcnt lgkmcnt(2)
	v_mul_f32_e32 v26, 0x42800000, v54
	v_med3_f32 v24, v24, s35, v84
	v_med3_f32 v26, v26, s35, v84
	v_cvt_pk_fp8_f32 v97, v24, v26
	s_waitcnt lgkmcnt(1)
	v_mul_f32_e32 v28, 0x42800000, v56
	s_waitcnt lgkmcnt(0)
	v_mul_f32_e32 v24, 0x42800000, v58
	v_med3_f32 v26, v28, s35, v84
	v_med3_f32 v24, v24, s35, v84
	v_cvt_pk_fp8_f32 v97, v26, v24 op_sel:[0,0,1]
	v_or_b32_e32 v24, s0, v63
	v_lshlrev_b32_e32 v60, 12, v24
	v_mul_f32_e32 v24, 0x42800000, v25
	v_mul_f32_e32 v25, 0x42800000, v27
	v_med3_f32 v27, v24, s35, v84
	v_med3_f32 v25, v25, s35, v84
	v_mov_b32_e32 v24, v3
	v_cvt_pk_fp8_f32 v24, v27, v25
	v_mul_f32_e32 v26, 0x42800000, v29
	v_mul_f32_e32 v25, 0x42800000, v31
	v_med3_f32 v26, v26, s35, v84
	v_med3_f32 v25, v25, s35, v84
	v_cvt_pk_fp8_f32 v24, v26, v25 op_sel:[0,0,1]
	v_mul_f32_e32 v25, 0x42800000, v37
	v_mul_f32_e32 v26, 0x42800000, v39
	v_med3_f32 v28, v25, s35, v84
	v_med3_f32 v26, v26, s35, v84
	v_mov_b32_e32 v25, v3
	v_cvt_pk_fp8_f32 v25, v28, v26
	v_mul_f32_e32 v27, 0x42800000, v41
	v_mul_f32_e32 v26, 0x42800000, v43
	v_med3_f32 v27, v27, s35, v84
	v_med3_f32 v26, v26, s35, v84
	v_cvt_pk_fp8_f32 v25, v27, v26 op_sel:[0,0,1]
	v_mul_f32_e32 v26, 0x42800000, v45
	v_mul_f32_e32 v27, 0x42800000, v47
	v_med3_f32 v29, v26, s35, v84
	v_med3_f32 v27, v27, s35, v84
	v_mov_b32_e32 v26, v3
	v_cvt_pk_fp8_f32 v26, v29, v27
	v_mul_f32_e32 v28, 0x42800000, v49
	v_mul_f32_e32 v27, 0x42800000, v51
	v_med3_f32 v28, v28, s35, v84
	v_med3_f32 v27, v27, s35, v84
	v_cvt_pk_fp8_f32 v26, v28, v27 op_sel:[0,0,1]
	v_mul_f32_e32 v27, 0x42800000, v53
	v_mul_f32_e32 v28, 0x42800000, v55
	v_med3_f32 v30, v27, s35, v84
	v_med3_f32 v28, v28, s35, v84
	v_mov_b32_e32 v27, v3
	v_cvt_pk_fp8_f32 v27, v30, v28
	v_mul_f32_e32 v29, 0x42800000, v57
	v_mul_f32_e32 v28, 0x42800000, v59
	v_med3_f32 v29, v29, s35, v84
	v_med3_f32 v28, v28, s35, v84
	v_cvt_pk_fp8_f32 v27, v29, v28 op_sel:[0,0,1]
	v_or_b32_e32 v28, s0, v65
	v_lshlrev_b32_e32 v28, 12, v28
	v_mov_b32_e32 v29, v3
	v_lshl_add_u64 v[60:61], v[32:33], 0, v[60:61]
	v_lshl_add_u64 v[28:29], v[32:33], 0, v[28:29]
	global_store_dwordx4 v[60:61], v[94:97], off
	global_store_dwordx4 v[28:29], v[24:27], off
	s_waitcnt lgkmcnt(0)

.LBB0_104:
	s_andn2_b64 vcc, exec, s[0:1]
	s_cbranch_vccnz .LBB0_106
	s_add_i32 s0, s3, 0x7600
	s_and_b32 s1, s0, 0xffff
	s_mul_i32 s1, s1, 0xbe83
	s_lshr_b32 s1, s1, 24
	s_mul_i32 s7, s1, 0x158
	s_sub_i32 s7, s0, s7
	s_lshl_b32 s0, s1, 6
	v_or_b32_e32 v24, s0, v35
	v_mul_u32_u24_e32 v24, 0x2b00, v24
	v_readlane_b32 s36, v247, 41
	v_lshlrev_b32_e32 v24, 2, v24
	v_mov_b32_e32 v25, v3
	v_readlane_b32 s48, v247, 53
	v_readlane_b32 s49, v247, 54
	s_lshl_b32 s1, s7, 7
	s_and_b32 s10, s1, 0x3ff80
	v_lshl_add_u64 v[24:25], s[48:49], 0, v[24:25]
	v_lshl_add_u64 v[24:25], v[24:25], 0, s[10:11]
	v_lshl_add_u64 v[32:33], v[24:25], 0, v[2:3]
	v_add_co_u32_e32 v28, vcc, s53, v32
	v_mov_b32_e32 v95, v3
	s_nop 0
	v_addc_co_u32_e32 v29, vcc, 0, v33, vcc
	v_add_co_u32_e32 v36, vcc, s54, v32
	s_nop 0
	v_addc_co_u32_e32 v37, vcc, 0, v33, vcc
	v_add_co_u32_e32 v40, vcc, s55, v32
	v_mov_b32_e32 v94, v3
	s_nop 0
	v_addc_co_u32_e32 v41, vcc, 0, v33, vcc
	v_add_co_u32_e32 v44, vcc, s56, v32
	s_nop 0
	v_addc_co_u32_e32 v45, vcc, 0, v33, vcc
	v_add_co_u32_e32 v48, vcc, s57, v32
	v_mov_b32_e32 v96, v3
	s_nop 0
	v_addc_co_u32_e32 v49, vcc, 0, v33, vcc
	s_nop 0
	v_add_co_u32_e32 v52, vcc, s58, v32
	s_mov_b32 s1, s11
	s_nop 0
	v_addc_co_u32_e32 v53, vcc, 0, v33, vcc
	v_add_co_u32_e32 v32, vcc, s59, v32
	v_mov_b32_e32 v97, v3
	s_nop 0
	v_addc_co_u32_e32 v33, vcc, 0, v33, vcc
	v_lshl_add_u64 v[32:33], v[6:7], 0, s[0:1]
	s_lshl_b32 s0, s7, 5
	s_lshl_b32 s1, s7, 6
	s_and_b32 s1, s1, 0x7f00
	s_and_b32 s0, s0, 0x60
	s_or_b32 s0, s1, s0
	s_and_b32 s0, s0, 0x7f60
	v_mov_b32_e32 v61, v3
	v_readlane_b32 s37, v247, 42
	v_readlane_b32 s38, v247, 43
	v_readlane_b32 s39, v247, 44
	v_readlane_b32 s40, v247, 45
	v_readlane_b32 s41, v247, 46
	v_readlane_b32 s42, v247, 47
	v_readlane_b32 s43, v247, 48
	v_readlane_b32 s44, v247, 49
	v_readlane_b32 s45, v247, 50
	v_readlane_b32 s46, v247, 51
	v_readlane_b32 s47, v247, 52
	v_readlane_b32 s50, v247, 55
	v_readlane_b32 s51, v247, 56
	s_waitcnt lgkmcnt(0)
	ds_read2_b32 v[24:25], v64 offset1:16
	ds_read2_b32 v[26:27], v64 offset0:33 offset1:49
	ds_read2_b32 v[28:29], v64 offset0:66 offset1:82
	ds_read2_b32 v[30:31], v64 offset0:99 offset1:115
	ds_read2_b32 v[36:37], v64 offset0:132 offset1:148
	ds_read2_b32 v[38:39], v64 offset0:165 offset1:181
	ds_read2_b32 v[40:41], v64 offset0:198 offset1:214
	ds_read2_b32 v[42:43], v64 offset0:231 offset1:247
	ds_read2_b32 v[44:45], v85 offset0:8 offset1:24
	s_waitcnt lgkmcnt(4)
	v_mul_f32_e32 v36, 0x42800000, v36
	s_waitcnt lgkmcnt(3)
	v_mul_f32_e32 v38, 0x42800000, v38
	v_med3_f32 v36, v36, s35, v84
	v_med3_f32 v38, v38, s35, v84
	v_cvt_pk_fp8_f32 v95, v36, v38
	v_mul_f32_e32 v24, 0x42800000, v24
	v_mul_f32_e32 v26, 0x42800000, v26
	ds_read2_b32 v[46:47], v85 offset0:41 offset1:57
	ds_read2_b32 v[48:49], v85 offset0:74 offset1:90
	ds_read2_b32 v[50:51], v85 offset0:107 offset1:123
	s_waitcnt lgkmcnt(5)
	v_mul_f32_e32 v40, 0x42800000, v40
	s_waitcnt lgkmcnt(4)
	v_mul_f32_e32 v42, 0x42800000, v42
	v_med3_f32 v24, v24, s35, v84
	v_med3_f32 v26, v26, s35, v84
	v_cvt_pk_fp8_f32 v94, v24, v26
	v_med3_f32 v24, v40, s35, v84
	v_med3_f32 v26, v42, s35, v84
	v_cvt_pk_fp8_f32 v95, v24, v26 op_sel:[0,0,1]
	s_waitcnt lgkmcnt(3)
	v_mul_f32_e32 v24, 0x42800000, v44
	s_waitcnt lgkmcnt(2)
	v_mul_f32_e32 v26, 0x42800000, v46
	v_med3_f32 v24, v24, s35, v84
	v_med3_f32 v26, v26, s35, v84
	v_mul_f32_e32 v28, 0x42800000, v28
	v_mul_f32_e32 v30, 0x42800000, v30
	v_cvt_pk_fp8_f32 v96, v24, v26
	ds_read2_b32 v[52:53], v85 offset0:140 offset1:156
	ds_read2_b32 v[54:55], v85 offset0:173 offset1:189
	ds_read2_b32 v[56:57], v85 offset0:206 offset1:222
	v_med3_f32 v28, v28, s35, v84
	v_med3_f32 v30, v30, s35, v84
	v_cvt_pk_fp8_f32 v94, v28, v30 op_sel:[0,0,1]
	s_waitcnt lgkmcnt(4)
	v_mul_f32_e32 v28, 0x42800000, v48
	s_waitcnt lgkmcnt(3)
	v_mul_f32_e32 v30, 0x42800000, v50
	v_med3_f32 v24, v28, s35, v84
	v_med3_f32 v26, v30, s35, v84
	ds_read2_b32 v[58:59], v85 offset0:239 offset1:255
	v_cvt_pk_fp8_f32 v96, v24, v26 op_sel:[0,0,1]
	s_waitcnt lgkmcnt(3)
	v_mul_f32_e32 v24, 0x42800000, v52
	s_waitcnt lgkmcnt(2)
	v_mul_f32_e32 v26, 0x42800000, v54
	v_med3_f32 v24, v24, s35, v84
	v_med3_f32 v26, v26, s35, v84
	v_cvt_pk_fp8_f32 v97, v24, v26
	s_waitcnt lgkmcnt(1)
	v_mul_f32_e32 v28, 0x42800000, v56
	s_waitcnt lgkmcnt(0)
	v_mul_f32_e32 v24, 0x42800000, v58
	v_med3_f32 v26, v28, s35, v84
	v_med3_f32 v24, v24, s35, v84
	v_cvt_pk_fp8_f32 v97, v26, v24 op_sel:[0,0,1]
	v_or_b32_e32 v24, s0, v63
	v_lshlrev_b32_e32 v60, 12, v24
	v_mul_f32_e32 v24, 0x42800000, v25
	v_mul_f32_e32 v25, 0x42800000, v27
	v_med3_f32 v27, v24, s35, v84
	v_med3_f32 v25, v25, s35, v84
	v_mov_b32_e32 v24, v3
	v_cvt_pk_fp8_f32 v24, v27, v25
	v_mul_f32_e32 v26, 0x42800000, v29
	v_mul_f32_e32 v25, 0x42800000, v31
	v_med3_f32 v26, v26, s35, v84
	v_med3_f32 v25, v25, s35, v84
	v_cvt_pk_fp8_f32 v24, v26, v25 op_sel:[0,0,1]
	v_mul_f32_e32 v25, 0x42800000, v37
	v_mul_f32_e32 v26, 0x42800000, v39
	v_med3_f32 v28, v25, s35, v84
	v_med3_f32 v26, v26, s35, v84
	v_mov_b32_e32 v25, v3
	v_cvt_pk_fp8_f32 v25, v28, v26
	v_mul_f32_e32 v27, 0x42800000, v41
	v_mul_f32_e32 v26, 0x42800000, v43
	v_med3_f32 v27, v27, s35, v84
	v_med3_f32 v26, v26, s35, v84
	v_cvt_pk_fp8_f32 v25, v27, v26 op_sel:[0,0,1]
	v_mul_f32_e32 v26, 0x42800000, v45
	v_mul_f32_e32 v27, 0x42800000, v47
	v_med3_f32 v29, v26, s35, v84
	v_med3_f32 v27, v27, s35, v84
	v_mov_b32_e32 v26, v3
	v_cvt_pk_fp8_f32 v26, v29, v27
	v_mul_f32_e32 v28, 0x42800000, v49
	v_mul_f32_e32 v27, 0x42800000, v51
	v_med3_f32 v28, v28, s35, v84
	v_med3_f32 v27, v27, s35, v84
	v_cvt_pk_fp8_f32 v26, v28, v27 op_sel:[0,0,1]
	v_mul_f32_e32 v27, 0x42800000, v53
	v_mul_f32_e32 v28, 0x42800000, v55
	v_med3_f32 v30, v27, s35, v84
	v_med3_f32 v28, v28, s35, v84
	v_mov_b32_e32 v27, v3
	v_cvt_pk_fp8_f32 v27, v30, v28
	v_mul_f32_e32 v29, 0x42800000, v57
	v_mul_f32_e32 v28, 0x42800000, v59
	v_med3_f32 v29, v29, s35, v84
	v_med3_f32 v28, v28, s35, v84
	v_cvt_pk_fp8_f32 v27, v29, v28 op_sel:[0,0,1]
	v_or_b32_e32 v28, s0, v65
	v_lshlrev_b32_e32 v28, 12, v28
	v_mov_b32_e32 v29, v3
	v_lshl_add_u64 v[60:61], v[32:33], 0, v[60:61]
	v_lshl_add_u64 v[28:29], v[32:33], 0, v[28:29]
	global_store_dwordx4 v[60:61], v[94:97], off
	global_store_dwordx4 v[28:29], v[24:27], off
	s_waitcnt lgkmcnt(0)

.LBB0_107:
	s_andn2_b64 vcc, exec, s[0:1]
	s_cbranch_vccnz .LBB0_109
	s_add_i32 s0, s3, 0x7a00
	s_lshr_b32 s0, s0, 1
	s_and_b32 s0, s0, 0x7fc0
	s_lshl_b32 s1, s3, 5
	v_or_b32_e32 v24, s0, v35
	v_readlane_b32 s36, v247, 41
	s_and_b32 s7, s1, 0xfe0
	v_lshlrev_b32_e32 v24, 14, v24
	v_mov_b32_e32 v25, v3
	v_readlane_b32 s44, v247, 49
	v_readlane_b32 s45, v247, 50
	s_lshl_b32 s10, s7, 2
	v_mov_b32_e32 v94, v3
	v_lshl_add_u64 v[24:25], s[44:45], 0, v[24:25]
	v_lshl_add_u64 v[24:25], v[24:25], 0, s[10:11]
	v_lshl_add_u64 v[32:33], v[24:25], 0, v[2:3]
	v_add_co_u32_e32 v28, vcc, s18, v32
	v_mov_b32_e32 v95, v3
	s_nop 0
	v_addc_co_u32_e32 v29, vcc, 0, v33, vcc
	v_add_co_u32_e32 v36, vcc, s19, v32
	s_nop 0
	v_addc_co_u32_e32 v37, vcc, 0, v33, vcc
	v_add_co_u32_e32 v40, vcc, s20, v32
	v_mov_b32_e32 v96, v3
	s_nop 0
	v_addc_co_u32_e32 v41, vcc, 0, v33, vcc
	v_add_co_u32_e32 v44, vcc, s21, v32
	s_nop 0
	v_addc_co_u32_e32 v45, vcc, 0, v33, vcc
	v_add_co_u32_e32 v48, vcc, s30, v32
	v_mov_b32_e32 v97, v3
	s_nop 0
	v_addc_co_u32_e32 v49, vcc, 0, v33, vcc
	s_nop 0
	v_add_co_u32_e32 v52, vcc, s31, v32
	s_mov_b32 s1, s11
	s_nop 0
	v_addc_co_u32_e32 v53, vcc, 0, v33, vcc
	v_add_co_u32_e32 v32, vcc, s34, v32
	v_mov_b32_e32 v61, v3
	s_nop 0
	v_addc_co_u32_e32 v33, vcc, 0, v33, vcc
	v_lshl_add_u64 v[32:33], v[8:9], 0, s[0:1]
	v_readlane_b32 s37, v247, 42
	v_readlane_b32 s38, v247, 43
	v_readlane_b32 s39, v247, 44
	v_readlane_b32 s40, v247, 45
	v_readlane_b32 s41, v247, 46
	v_readlane_b32 s42, v247, 47
	v_readlane_b32 s43, v247, 48
	v_readlane_b32 s46, v247, 51
	v_readlane_b32 s47, v247, 52
	v_readlane_b32 s48, v247, 53
	v_readlane_b32 s49, v247, 54
	v_readlane_b32 s50, v247, 55
	v_readlane_b32 s51, v247, 56
	s_waitcnt lgkmcnt(0)
	ds_read2_b32 v[24:25], v64 offset1:16
	ds_read2_b32 v[26:27], v64 offset0:33 offset1:49
	ds_read2_b32 v[28:29], v64 offset0:66 offset1:82
	ds_read2_b32 v[30:31], v64 offset0:99 offset1:115
	ds_read2_b32 v[36:37], v64 offset0:132 offset1:148
	ds_read2_b32 v[38:39], v64 offset0:165 offset1:181
	ds_read2_b32 v[40:41], v64 offset0:198 offset1:214
	ds_read2_b32 v[42:43], v64 offset0:231 offset1:247
	ds_read2_b32 v[44:45], v85 offset0:8 offset1:24
	ds_read2_b32 v[46:47], v85 offset0:41 offset1:57
	ds_read2_b32 v[48:49], v85 offset0:74 offset1:90
	ds_read2_b32 v[50:51], v85 offset0:107 offset1:123
	s_waitcnt lgkmcnt(11)
	v_mul_f32_e32 v24, 0x42800000, v24
	s_waitcnt lgkmcnt(10)
	v_mul_f32_e32 v26, 0x42800000, v26
	s_waitcnt lgkmcnt(7)
	v_mul_f32_e32 v36, 0x42800000, v36
	s_waitcnt lgkmcnt(6)
	v_mul_f32_e32 v38, 0x42800000, v38
	v_med3_f32 v24, v24, s35, v84
	v_med3_f32 v26, v26, s35, v84
	v_med3_f32 v36, v36, s35, v84
	v_med3_f32 v38, v38, s35, v84
	v_cvt_pk_fp8_f32 v94, v24, v26
	v_cvt_pk_fp8_f32 v95, v36, v38
	v_mul_f32_e32 v28, 0x42800000, v28
	v_mul_f32_e32 v30, 0x42800000, v30
	s_waitcnt lgkmcnt(5)
	v_mul_f32_e32 v40, 0x42800000, v40
	s_waitcnt lgkmcnt(4)
	v_mul_f32_e32 v42, 0x42800000, v42
	s_waitcnt lgkmcnt(3)
	v_mul_f32_e32 v44, 0x42800000, v44
	s_waitcnt lgkmcnt(2)
	v_mul_f32_e32 v46, 0x42800000, v46
	v_med3_f32 v28, v28, s35, v84
	v_med3_f32 v30, v30, s35, v84
	v_med3_f32 v24, v40, s35, v84
	v_med3_f32 v26, v42, s35, v84
	v_cvt_pk_fp8_f32 v94, v28, v30 op_sel:[0,0,1]
	v_cvt_pk_fp8_f32 v95, v24, v26 op_sel:[0,0,1]
	v_med3_f32 v26, v44, s35, v84
	v_med3_f32 v28, v46, s35, v84
	v_cvt_pk_fp8_f32 v96, v26, v28
	ds_read2_b32 v[52:53], v85 offset0:140 offset1:156
	ds_read2_b32 v[54:55], v85 offset0:173 offset1:189
	ds_read2_b32 v[56:57], v85 offset0:206 offset1:222
	s_waitcnt lgkmcnt(4)
	v_mul_f32_e32 v48, 0x42800000, v48
	s_waitcnt lgkmcnt(3)
	v_mul_f32_e32 v24, 0x42800000, v50
	v_med3_f32 v26, v48, s35, v84
	v_med3_f32 v24, v24, s35, v84
	ds_read2_b32 v[58:59], v85 offset0:239 offset1:255
	v_cvt_pk_fp8_f32 v96, v26, v24 op_sel:[0,0,1]
	s_waitcnt lgkmcnt(3)
	v_mul_f32_e32 v24, 0x42800000, v52
	s_waitcnt lgkmcnt(2)
	v_mul_f32_e32 v26, 0x42800000, v54
	v_med3_f32 v24, v24, s35, v84
	v_med3_f32 v26, v26, s35, v84
	v_cvt_pk_fp8_f32 v97, v24, v26
	s_waitcnt lgkmcnt(1)
	v_mul_f32_e32 v28, 0x42800000, v56
	s_waitcnt lgkmcnt(0)
	v_mul_f32_e32 v24, 0x42800000, v58
	v_med3_f32 v26, v28, s35, v84
	v_med3_f32 v24, v24, s35, v84
	v_cvt_pk_fp8_f32 v97, v26, v24 op_sel:[0,0,1]
	v_or_b32_e32 v24, s7, v63
	v_lshlrev_b32_e32 v60, 9, v24
	v_mul_f32_e32 v24, 0x42800000, v25
	v_mul_f32_e32 v25, 0x42800000, v27
	v_med3_f32 v27, v24, s35, v84
	v_med3_f32 v25, v25, s35, v84
	v_mov_b32_e32 v24, v3
	v_cvt_pk_fp8_f32 v24, v27, v25
	v_mul_f32_e32 v26, 0x42800000, v29
	v_mul_f32_e32 v25, 0x42800000, v31
	v_med3_f32 v26, v26, s35, v84
	v_med3_f32 v25, v25, s35, v84
	v_cvt_pk_fp8_f32 v24, v26, v25 op_sel:[0,0,1]
	v_mul_f32_e32 v25, 0x42800000, v37
	v_mul_f32_e32 v26, 0x42800000, v39
	v_med3_f32 v28, v25, s35, v84
	v_med3_f32 v26, v26, s35, v84
	v_mov_b32_e32 v25, v3
	v_cvt_pk_fp8_f32 v25, v28, v26
	v_mul_f32_e32 v27, 0x42800000, v41
	v_mul_f32_e32 v26, 0x42800000, v43
	v_med3_f32 v27, v27, s35, v84
	v_med3_f32 v26, v26, s35, v84
	v_cvt_pk_fp8_f32 v25, v27, v26 op_sel:[0,0,1]
	v_mul_f32_e32 v26, 0x42800000, v45
	v_mul_f32_e32 v27, 0x42800000, v47
	v_med3_f32 v29, v26, s35, v84
	v_med3_f32 v27, v27, s35, v84
	v_mov_b32_e32 v26, v3
	v_cvt_pk_fp8_f32 v26, v29, v27
	v_mul_f32_e32 v28, 0x42800000, v49
	v_mul_f32_e32 v27, 0x42800000, v51
	v_med3_f32 v28, v28, s35, v84
	v_med3_f32 v27, v27, s35, v84
	v_cvt_pk_fp8_f32 v26, v28, v27 op_sel:[0,0,1]
	v_mul_f32_e32 v27, 0x42800000, v53
	v_mul_f32_e32 v28, 0x42800000, v55
	v_med3_f32 v30, v27, s35, v84
	v_med3_f32 v28, v28, s35, v84
	v_mov_b32_e32 v27, v3
	v_cvt_pk_fp8_f32 v27, v30, v28
	v_mul_f32_e32 v29, 0x42800000, v57
	v_mul_f32_e32 v28, 0x42800000, v59
	v_med3_f32 v29, v29, s35, v84
	v_med3_f32 v28, v28, s35, v84
	v_cvt_pk_fp8_f32 v27, v29, v28 op_sel:[0,0,1]
	v_or_b32_e32 v28, s7, v65
	v_lshlrev_b32_e32 v28, 9, v28
	v_mov_b32_e32 v29, v3
	v_lshl_add_u64 v[60:61], v[32:33], 0, v[60:61]
	v_lshl_add_u64 v[28:29], v[32:33], 0, v[28:29]
	global_store_dwordx4 v[60:61], v[94:97], off
	global_store_dwordx4 v[28:29], v[24:27], off
	s_waitcnt lgkmcnt(0)

.LBB0_110:
	s_andn2_b64 vcc, exec, s[0:1]
	s_cbranch_vccnz .LBB0_112
	s_and_b32 s1, s16, 0x3ffc0
	s_lshl_b32 s0, s3, 5
	v_or_b32_e32 v24, s1, v35
	v_readlane_b32 s36, v247, 41
	s_and_b32 s7, s0, 0x1e0
	v_lshlrev_b32_e32 v24, 11, v24
	v_mov_b32_e32 v25, v3
	v_readlane_b32 s42, v247, 47
	v_readlane_b32 s43, v247, 48
	s_lshl_b32 s10, s7, 2
	s_bitset1_b32 s0, 9
	v_lshl_add_u64 v[24:25], s[42:43], 0, v[24:25]
	v_lshl_add_u64 v[24:25], v[24:25], 0, s[10:11]
	v_lshl_add_u64 v[32:33], v[24:25], 0, v[2:3]
	v_add_co_u32_e32 v28, vcc, s72, v32
	s_and_b32 s0, s0, 0x3e0
	s_nop 0
	v_addc_co_u32_e32 v29, vcc, 0, v33, vcc
	v_add_co_u32_e32 v36, vcc, s73, v32
	s_nop 0
	v_addc_co_u32_e32 v37, vcc, 0, v33, vcc
	v_add_co_u32_e32 v40, vcc, s74, v32
	s_lshl_b32 s10, s1, 1
	s_nop 0
	v_addc_co_u32_e32 v41, vcc, 0, v33, vcc
	v_add_co_u32_e32 v44, vcc, s75, v32
	s_nop 0
	v_addc_co_u32_e32 v45, vcc, 0, v33, vcc
	v_add_co_u32_e32 v48, vcc, s64, v32
	v_readlane_b32 s37, v247, 42
	s_nop 0
	v_addc_co_u32_e32 v49, vcc, 0, v33, vcc
	s_nop 0
	v_add_co_u32_e32 v52, vcc, s65, v32
	v_readlane_b32 s38, v247, 43
	s_nop 0
	v_addc_co_u32_e32 v53, vcc, 0, v33, vcc
	v_add_co_u32_e32 v32, vcc, s66, v32
	v_readlane_b32 s39, v247, 44
	s_nop 0
	v_addc_co_u32_e32 v33, vcc, 0, v33, vcc
	v_lshl_add_u64 v[32:33], v[10:11], 0, s[10:11]
	v_readlane_b32 s40, v247, 45
	v_readlane_b32 s41, v247, 46
	v_readlane_b32 s44, v247, 49
	v_readlane_b32 s45, v247, 50
	v_readlane_b32 s46, v247, 51
	v_readlane_b32 s47, v247, 52
	v_readlane_b32 s48, v247, 53
	v_readlane_b32 s49, v247, 54
	v_readlane_b32 s50, v247, 55
	v_readlane_b32 s51, v247, 56
	s_waitcnt lgkmcnt(0)
	ds_read2_b32 v[28:29], v66 offset0:33 offset1:41
	ds_read2_b32 v[30:31], v66 offset1:8
	ds_read2_b32 v[36:37], v66 offset0:66 offset1:74
	ds_read2_b32 v[38:39], v66 offset0:99 offset1:107
	ds_read2_b32 v[40:41], v66 offset0:132 offset1:140
	ds_read2_b32 v[42:43], v66 offset0:165 offset1:173
	ds_read2_b32 v[44:45], v66 offset0:198 offset1:206
	ds_read2_b32 v[46:47], v66 offset0:231 offset1:239
	s_waitcnt lgkmcnt(6)
	v_bfe_u32 v24, v30, 16, 1
	v_bfe_u32 v25, v28, 16, 1
	s_waitcnt lgkmcnt(5)
	v_bfe_u32 v26, v36, 16, 1
	s_waitcnt lgkmcnt(3)
	v_bfe_u32 v48, v40, 16, 1
	v_bfe_u32 v27, v38, 16, 1
	s_waitcnt lgkmcnt(2)
	v_bfe_u32 v49, v42, 16, 1
	v_add3_u32 v24, v30, v24, s67
	v_add3_u32 v25, v28, v25, s67
	v_add3_u32 v26, v36, v26, s67
	v_add3_u32 v28, v40, v48, s67
	s_waitcnt lgkmcnt(1)
	v_bfe_u32 v50, v44, 16, 1
	v_add3_u32 v27, v38, v27, s67
	v_add3_u32 v30, v42, v49, s67
	v_lshrrev_b32_e32 v24, 16, v24
	v_lshrrev_b32_e32 v26, 16, v26
	v_lshrrev_b32_e32 v28, 16, v28
	s_waitcnt lgkmcnt(0)
	v_bfe_u32 v51, v46, 16, 1
	v_add3_u32 v36, v44, v50, s67
	v_and_or_b32 v24, v25, s68, v24
	v_and_or_b32 v25, v27, s68, v26
	v_and_or_b32 v26, v30, s68, v28
	v_or_b32_e32 v28, s0, v35
	v_add3_u32 v38, v46, v51, s67
	v_lshrrev_b32_e32 v36, 16, v36
	v_lshlrev_b32_e32 v48, 13, v28
	v_mov_b32_e32 v49, v3
	v_and_or_b32 v27, v38, s68, v36
	v_lshl_add_u64 v[48:49], v[32:33], 0, v[48:49]
	global_store_dwordx4 v[48:49], v[24:27], off
	v_bfe_u32 v28, v47, 16, 1
	v_add3_u32 v28, v47, v28, s67
	v_bfe_u32 v24, v31, 16, 1
	v_add3_u32 v24, v31, v24, s67
	v_bfe_u32 v25, v29, 16, 1
	v_lshrrev_b32_e32 v24, 16, v24
	v_add3_u32 v25, v29, v25, s67
	v_and_or_b32 v24, v25, s68, v24
	v_bfe_u32 v25, v37, 16, 1
	v_add3_u32 v25, v37, v25, s67
	v_bfe_u32 v26, v39, 16, 1
	v_lshrrev_b32_e32 v25, 16, v25
	v_add3_u32 v26, v39, v26, s67
	v_and_or_b32 v25, v26, s68, v25
	v_bfe_u32 v26, v41, 16, 1
	v_add3_u32 v26, v41, v26, s67
	v_bfe_u32 v27, v43, 16, 1
	v_lshrrev_b32_e32 v26, 16, v26
	v_add3_u32 v27, v43, v27, s67
	v_and_or_b32 v26, v27, s68, v26
	v_bfe_u32 v27, v45, 16, 1
	v_add3_u32 v27, v45, v27, s67
	v_lshrrev_b32_e32 v27, 16, v27
	v_and_or_b32 v27, v28, s68, v27
	v_or_b32_e32 v28, s0, v67
	v_lshlrev_b32_e32 v28, 13, v28
	v_mov_b32_e32 v29, v3
	ds_read2_b32 v[30:31], v66 offset0:16 offset1:24
	v_lshl_add_u64 v[28:29], v[32:33], 0, v[28:29]
	global_store_dwordx4 v[28:29], v[24:27], off
	ds_read2_b32 v[28:29], v66 offset0:49 offset1:57
	ds_read2_b32 v[36:37], v66 offset0:82 offset1:90
	ds_read2_b32 v[38:39], v66 offset0:115 offset1:123
	s_waitcnt lgkmcnt(3)
	v_bfe_u32 v24, v30, 16, 1
	v_add3_u32 v24, v30, v24, s67
	s_waitcnt lgkmcnt(2)
	v_bfe_u32 v25, v28, 16, 1
	ds_read2_b32 v[40:41], v66 offset0:148 offset1:156
	v_lshrrev_b32_e32 v24, 16, v24
	v_add3_u32 v25, v28, v25, s67
	ds_read2_b32 v[42:43], v66 offset0:181 offset1:189
	v_and_or_b32 v24, v25, s68, v24
	s_waitcnt lgkmcnt(3)
	v_bfe_u32 v25, v36, 16, 1
	v_add3_u32 v25, v36, v25, s67
	s_waitcnt lgkmcnt(2)
	v_bfe_u32 v26, v38, 16, 1
	ds_read2_b32 v[44:45], v66 offset0:214 offset1:222
	v_lshrrev_b32_e32 v25, 16, v25
	v_add3_u32 v26, v38, v26, s67
	ds_read2_b32 v[46:47], v66 offset0:247 offset1:255
	v_and_or_b32 v25, v26, s68, v25
	s_waitcnt lgkmcnt(3)
	v_bfe_u32 v26, v40, 16, 1
	v_add3_u32 v26, v40, v26, s67
	s_waitcnt lgkmcnt(2)
	v_bfe_u32 v27, v42, 16, 1
	v_lshrrev_b32_e32 v26, 16, v26
	v_add3_u32 v27, v42, v27, s67
	v_and_or_b32 v26, v27, s68, v26
	s_waitcnt lgkmcnt(1)
	v_bfe_u32 v27, v44, 16, 1
	v_add3_u32 v27, v44, v27, s67
	s_waitcnt lgkmcnt(0)
	v_bfe_u32 v28, v46, 16, 1
	v_lshrrev_b32_e32 v27, 16, v27
	v_add3_u32 v28, v46, v28, s67
	v_and_or_b32 v27, v28, s68, v27
	v_or_b32_e32 v28, s0, v68
	v_lshlrev_b32_e32 v48, 13, v28
	v_mov_b32_e32 v49, v3
	v_lshl_add_u64 v[48:49], v[32:33], 0, v[48:49]
	global_store_dwordx4 v[48:49], v[24:27], off
	v_bfe_u32 v28, v47, 16, 1
	v_add3_u32 v28, v47, v28, s67
	v_bfe_u32 v24, v31, 16, 1
	v_add3_u32 v24, v31, v24, s67
	v_bfe_u32 v25, v29, 16, 1
	v_lshrrev_b32_e32 v24, 16, v24
	v_add3_u32 v25, v29, v25, s67
	v_and_or_b32 v24, v25, s68, v24
	v_bfe_u32 v25, v37, 16, 1
	v_add3_u32 v25, v37, v25, s67
	v_bfe_u32 v26, v39, 16, 1
	v_lshrrev_b32_e32 v25, 16, v25
	v_add3_u32 v26, v39, v26, s67
	v_and_or_b32 v25, v26, s68, v25
	v_bfe_u32 v26, v41, 16, 1
	v_add3_u32 v26, v41, v26, s67
	v_bfe_u32 v27, v43, 16, 1
	v_lshrrev_b32_e32 v26, 16, v26
	v_add3_u32 v27, v43, v27, s67
	v_and_or_b32 v26, v27, s68, v26
	v_bfe_u32 v27, v45, 16, 1
	v_add3_u32 v27, v45, v27, s67
	v_lshrrev_b32_e32 v27, 16, v27
	v_and_or_b32 v27, v28, s68, v27
	v_or_b32_e32 v28, s0, v69
	v_lshlrev_b32_e32 v28, 13, v28
	v_mov_b32_e32 v29, v3
	v_lshl_add_u64 v[28:29], v[32:33], 0, v[28:29]
	global_store_dwordx4 v[28:29], v[24:27], off
	s_waitcnt lgkmcnt(0)

.LBB0_113:
	s_andn2_b64 vcc, exec, s[0:1]
	s_cbranch_vccnz .LBB0_115
	s_add_i32 s0, s16, 0x1000
	s_and_b32 s1, s0, 0x3ffc0
	s_lshl_b32 s0, s3, 5
	v_or_b32_e32 v24, s1, v35
	v_readlane_b32 s36, v247, 41
	s_and_b32 s0, s0, 0x1e0
	v_lshlrev_b32_e32 v24, 11, v24
	v_mov_b32_e32 v25, v3
	v_readlane_b32 s40, v247, 45
	v_readlane_b32 s41, v247, 46
	s_lshl_b32 s10, s0, 2
	v_readlane_b32 s37, v247, 42
	v_lshl_add_u64 v[24:25], s[40:41], 0, v[24:25]
	v_lshl_add_u64 v[24:25], v[24:25], 0, s[10:11]
	v_lshl_add_u64 v[32:33], v[24:25], 0, v[2:3]
	v_add_co_u32_e32 v28, vcc, s72, v32
	s_lshl_b32 s10, s1, 1
	s_nop 0
	v_addc_co_u32_e32 v29, vcc, 0, v33, vcc
	v_add_co_u32_e32 v36, vcc, s73, v32
	s_nop 0
	v_addc_co_u32_e32 v37, vcc, 0, v33, vcc
	v_add_co_u32_e32 v40, vcc, s74, v32
	v_lshl_add_u64 v[60:61], v[10:11], 0, s[10:11]
	s_nop 0
	v_addc_co_u32_e32 v41, vcc, 0, v33, vcc
	v_add_co_u32_e32 v44, vcc, s75, v32
	s_nop 0
	v_addc_co_u32_e32 v45, vcc, 0, v33, vcc
	v_add_co_u32_e32 v48, vcc, s64, v32
	v_readlane_b32 s38, v247, 43
	s_nop 0
	v_addc_co_u32_e32 v49, vcc, 0, v33, vcc
	s_nop 0
	v_add_co_u32_e32 v52, vcc, s65, v32
	v_readlane_b32 s39, v247, 44
	s_nop 0
	v_addc_co_u32_e32 v53, vcc, 0, v33, vcc
	v_add_co_u32_e32 v32, vcc, s66, v32
	v_readlane_b32 s42, v247, 47
	s_nop 0
	v_addc_co_u32_e32 v33, vcc, 0, v33, vcc
	v_or_b32_e32 v32, s0, v35
	v_lshlrev_b32_e32 v32, 13, v32
	v_readlane_b32 s43, v247, 48
	v_readlane_b32 s44, v247, 49
	v_readlane_b32 s45, v247, 50
	v_readlane_b32 s46, v247, 51
	v_readlane_b32 s47, v247, 52
	v_readlane_b32 s48, v247, 53
	v_readlane_b32 s49, v247, 54
	v_readlane_b32 s50, v247, 55
	v_readlane_b32 s51, v247, 56
	s_waitcnt lgkmcnt(0)
	ds_read2_b32 v[28:29], v66 offset0:33 offset1:41
	ds_read2_b32 v[30:31], v66 offset1:8
	ds_read2_b32 v[36:37], v66 offset0:66 offset1:74
	ds_read2_b32 v[38:39], v66 offset0:99 offset1:107
	ds_read2_b32 v[40:41], v66 offset0:132 offset1:140
	ds_read2_b32 v[42:43], v66 offset0:165 offset1:173
	ds_read2_b32 v[44:45], v66 offset0:198 offset1:206
	ds_read2_b32 v[46:47], v66 offset0:231 offset1:239
	s_waitcnt lgkmcnt(6)
	v_bfe_u32 v24, v30, 16, 1
	v_bfe_u32 v25, v28, 16, 1
	s_waitcnt lgkmcnt(5)
	v_bfe_u32 v26, v36, 16, 1
	s_waitcnt lgkmcnt(3)
	v_bfe_u32 v33, v40, 16, 1
	s_waitcnt lgkmcnt(1)
	v_bfe_u32 v49, v44, 16, 1
	v_bfe_u32 v27, v38, 16, 1
	s_waitcnt lgkmcnt(0)
	v_bfe_u32 v50, v46, 16, 1
	v_add3_u32 v24, v30, v24, s67
	v_add3_u32 v25, v28, v25, s67
	v_add3_u32 v26, v36, v26, s67
	v_add3_u32 v28, v40, v33, s67
	v_add3_u32 v33, v44, v49, s67
	v_bfe_u32 v48, v42, 16, 1
	v_add3_u32 v27, v38, v27, s67
	v_add3_u32 v36, v46, v50, s67
	v_lshrrev_b32_e32 v24, 16, v24
	v_lshrrev_b32_e32 v26, 16, v26
	v_lshrrev_b32_e32 v33, 16, v33
	v_add3_u32 v30, v42, v48, s67
	v_lshrrev_b32_e32 v28, 16, v28
	v_and_or_b32 v24, v25, s68, v24
	v_and_or_b32 v25, v27, s68, v26
	v_and_or_b32 v27, v36, s68, v33
	v_mov_b32_e32 v33, v3
	v_and_or_b32 v26, v30, s68, v28
	v_lshl_add_u64 v[32:33], v[60:61], 0, v[32:33]
	global_store_dwordx4 v[32:33], v[24:27], off
	v_bfe_u32 v28, v47, 16, 1
	v_add3_u32 v28, v47, v28, s67
	v_bfe_u32 v24, v31, 16, 1
	v_add3_u32 v24, v31, v24, s67
	v_bfe_u32 v25, v29, 16, 1
	v_lshrrev_b32_e32 v24, 16, v24
	v_add3_u32 v25, v29, v25, s67
	v_and_or_b32 v24, v25, s68, v24
	v_bfe_u32 v25, v37, 16, 1
	v_add3_u32 v25, v37, v25, s67
	v_bfe_u32 v26, v39, 16, 1
	v_lshrrev_b32_e32 v25, 16, v25
	v_add3_u32 v26, v39, v26, s67
	v_and_or_b32 v25, v26, s68, v25
	v_bfe_u32 v26, v41, 16, 1
	v_add3_u32 v26, v41, v26, s67
	v_bfe_u32 v27, v43, 16, 1
	v_lshrrev_b32_e32 v26, 16, v26
	v_add3_u32 v27, v43, v27, s67
	v_and_or_b32 v26, v27, s68, v26
	v_bfe_u32 v27, v45, 16, 1
	v_add3_u32 v27, v45, v27, s67
	v_lshrrev_b32_e32 v27, 16, v27
	v_and_or_b32 v27, v28, s68, v27
	v_or_b32_e32 v28, s0, v67
	v_lshlrev_b32_e32 v28, 13, v28
	v_mov_b32_e32 v29, v3
	ds_read2_b32 v[30:31], v66 offset0:16 offset1:24
	v_lshl_add_u64 v[28:29], v[60:61], 0, v[28:29]
	global_store_dwordx4 v[28:29], v[24:27], off
	ds_read2_b32 v[28:29], v66 offset0:49 offset1:57
	ds_read2_b32 v[32:33], v66 offset0:82 offset1:90
	ds_read2_b32 v[36:37], v66 offset0:115 offset1:123
	s_waitcnt lgkmcnt(3)
	v_bfe_u32 v24, v30, 16, 1
	v_add3_u32 v24, v30, v24, s67
	s_waitcnt lgkmcnt(2)
	v_bfe_u32 v25, v28, 16, 1
	ds_read2_b32 v[38:39], v66 offset0:148 offset1:156
	v_lshrrev_b32_e32 v24, 16, v24
	v_add3_u32 v25, v28, v25, s67
	ds_read2_b32 v[40:41], v66 offset0:181 offset1:189
	v_and_or_b32 v24, v25, s68, v24
	s_waitcnt lgkmcnt(3)
	v_bfe_u32 v25, v32, 16, 1
	v_add3_u32 v25, v32, v25, s67
	s_waitcnt lgkmcnt(2)
	v_bfe_u32 v26, v36, 16, 1
	ds_read2_b32 v[42:43], v66 offset0:214 offset1:222
	v_lshrrev_b32_e32 v25, 16, v25
	v_add3_u32 v26, v36, v26, s67
	ds_read2_b32 v[44:45], v66 offset0:247 offset1:255
	v_and_or_b32 v25, v26, s68, v25
	s_waitcnt lgkmcnt(3)
	v_bfe_u32 v26, v38, 16, 1
	v_add3_u32 v26, v38, v26, s67
	s_waitcnt lgkmcnt(2)
	v_bfe_u32 v27, v40, 16, 1
	v_lshrrev_b32_e32 v26, 16, v26
	v_add3_u32 v27, v40, v27, s67
	v_and_or_b32 v26, v27, s68, v26
	s_waitcnt lgkmcnt(1)
	v_bfe_u32 v27, v42, 16, 1
	v_add3_u32 v27, v42, v27, s67
	s_waitcnt lgkmcnt(0)
	v_bfe_u32 v28, v44, 16, 1
	v_lshrrev_b32_e32 v27, 16, v27
	v_add3_u32 v28, v44, v28, s67
	v_and_or_b32 v27, v28, s68, v27
	v_or_b32_e32 v28, s0, v68
	v_lshlrev_b32_e32 v46, 13, v28
	v_mov_b32_e32 v47, v3
	v_lshl_add_u64 v[46:47], v[60:61], 0, v[46:47]
	global_store_dwordx4 v[46:47], v[24:27], off
	v_bfe_u32 v28, v45, 16, 1
	v_add3_u32 v28, v45, v28, s67
	v_bfe_u32 v24, v31, 16, 1
	v_add3_u32 v24, v31, v24, s67
	v_bfe_u32 v25, v29, 16, 1
	v_lshrrev_b32_e32 v24, 16, v24
	v_add3_u32 v25, v29, v25, s67
	v_and_or_b32 v24, v25, s68, v24
	v_bfe_u32 v25, v33, 16, 1
	v_add3_u32 v25, v33, v25, s67
	v_bfe_u32 v26, v37, 16, 1
	v_lshrrev_b32_e32 v25, 16, v25
	v_add3_u32 v26, v37, v26, s67
	v_and_or_b32 v25, v26, s68, v25
	v_bfe_u32 v26, v39, 16, 1
	v_add3_u32 v26, v39, v26, s67
	v_bfe_u32 v27, v41, 16, 1
	v_lshrrev_b32_e32 v26, 16, v26
	v_add3_u32 v27, v41, v27, s67
	v_and_or_b32 v26, v27, s68, v26
	v_bfe_u32 v27, v43, 16, 1
	v_add3_u32 v27, v43, v27, s67
	v_lshrrev_b32_e32 v27, 16, v27
	v_and_or_b32 v27, v28, s68, v27
	v_or_b32_e32 v28, s0, v69
	v_lshlrev_b32_e32 v28, 13, v28
	v_mov_b32_e32 v29, v3
	v_lshl_add_u64 v[28:29], v[60:61], 0, v[28:29]
	global_store_dwordx4 v[28:29], v[24:27], off
	s_waitcnt lgkmcnt(0)

.LBB0_116:
	s_andn2_b64 vcc, exec, s[0:1]
	s_cbranch_vccnz .LBB0_118
	s_add_i32 s0, s16, 0x2000
	s_and_b32 s0, s0, 0x3ffc0
	s_lshl_b32 s1, s3, 5
	v_or_b32_e32 v24, s0, v35
	v_readlane_b32 s36, v247, 41
	s_and_b32 s7, s1, 0x1e0
	v_lshlrev_b32_e32 v24, 11, v24
	v_mov_b32_e32 v25, v3
	v_readlane_b32 s38, v247, 43
	v_readlane_b32 s39, v247, 44
	s_lshl_b32 s10, s7, 2
	v_mov_b32_e32 v94, v3
	v_lshl_add_u64 v[24:25], s[38:39], 0, v[24:25]
	v_lshl_add_u64 v[24:25], v[24:25], 0, s[10:11]
	v_lshl_add_u64 v[32:33], v[24:25], 0, v[2:3]
	v_add_co_u32_e32 v28, vcc, s72, v32
	v_mov_b32_e32 v95, v3
	s_nop 0
	v_addc_co_u32_e32 v29, vcc, 0, v33, vcc
	v_add_co_u32_e32 v36, vcc, s73, v32
	s_nop 0
	v_addc_co_u32_e32 v37, vcc, 0, v33, vcc
	v_add_co_u32_e32 v40, vcc, s74, v32
	v_mov_b32_e32 v96, v3
	s_nop 0
	v_addc_co_u32_e32 v41, vcc, 0, v33, vcc
	v_add_co_u32_e32 v44, vcc, s75, v32
	s_nop 0
	v_addc_co_u32_e32 v45, vcc, 0, v33, vcc
	v_add_co_u32_e32 v48, vcc, s64, v32
	v_mov_b32_e32 v97, v3
	s_nop 0
	v_addc_co_u32_e32 v49, vcc, 0, v33, vcc
	s_nop 0
	v_add_co_u32_e32 v52, vcc, s65, v32
	s_mov_b32 s1, s11
	s_nop 0
	v_addc_co_u32_e32 v53, vcc, 0, v33, vcc
	v_add_co_u32_e32 v32, vcc, s66, v32
	v_mov_b32_e32 v61, v3
	s_nop 0
	v_addc_co_u32_e32 v33, vcc, 0, v33, vcc
	v_lshl_add_u64 v[32:33], v[12:13], 0, s[0:1]
	v_readlane_b32 s37, v247, 42
	v_readlane_b32 s40, v247, 45
	v_readlane_b32 s41, v247, 46
	v_readlane_b32 s42, v247, 47
	v_readlane_b32 s43, v247, 48
	v_readlane_b32 s44, v247, 49
	v_readlane_b32 s45, v247, 50
	v_readlane_b32 s46, v247, 51
	v_readlane_b32 s47, v247, 52
	v_readlane_b32 s48, v247, 53
	v_readlane_b32 s49, v247, 54
	v_readlane_b32 s50, v247, 55
	v_readlane_b32 s51, v247, 56
	s_waitcnt lgkmcnt(0)
	ds_read2_b32 v[24:25], v64 offset1:16
	ds_read2_b32 v[26:27], v64 offset0:33 offset1:49
	ds_read2_b32 v[28:29], v64 offset0:66 offset1:82
	ds_read2_b32 v[30:31], v64 offset0:99 offset1:115
	ds_read2_b32 v[36:37], v64 offset0:132 offset1:148
	ds_read2_b32 v[38:39], v64 offset0:165 offset1:181
	ds_read2_b32 v[40:41], v64 offset0:198 offset1:214
	ds_read2_b32 v[42:43], v64 offset0:231 offset1:247
	ds_read2_b32 v[44:45], v85 offset0:8 offset1:24
	ds_read2_b32 v[46:47], v85 offset0:41 offset1:57
	ds_read2_b32 v[48:49], v85 offset0:74 offset1:90
	ds_read2_b32 v[50:51], v85 offset0:107 offset1:123
	s_waitcnt lgkmcnt(11)
	v_mul_f32_e32 v24, 0x42800000, v24
	s_waitcnt lgkmcnt(10)
	v_mul_f32_e32 v26, 0x42800000, v26
	s_waitcnt lgkmcnt(7)
	v_mul_f32_e32 v36, 0x42800000, v36
	s_waitcnt lgkmcnt(6)
	v_mul_f32_e32 v38, 0x42800000, v38
	v_med3_f32 v24, v24, s35, v84
	v_med3_f32 v26, v26, s35, v84
	v_med3_f32 v36, v36, s35, v84
	v_med3_f32 v38, v38, s35, v84
	v_cvt_pk_fp8_f32 v94, v24, v26
	v_cvt_pk_fp8_f32 v95, v36, v38
	v_mul_f32_e32 v28, 0x42800000, v28
	v_mul_f32_e32 v30, 0x42800000, v30
	s_waitcnt lgkmcnt(5)
	v_mul_f32_e32 v40, 0x42800000, v40
	s_waitcnt lgkmcnt(4)
	v_mul_f32_e32 v42, 0x42800000, v42
	s_waitcnt lgkmcnt(3)
	v_mul_f32_e32 v44, 0x42800000, v44
	s_waitcnt lgkmcnt(2)
	v_mul_f32_e32 v46, 0x42800000, v46
	v_med3_f32 v28, v28, s35, v84
	v_med3_f32 v30, v30, s35, v84
	v_med3_f32 v24, v40, s35, v84
	v_med3_f32 v26, v42, s35, v84
	v_cvt_pk_fp8_f32 v94, v28, v30 op_sel:[0,0,1]
	v_cvt_pk_fp8_f32 v95, v24, v26 op_sel:[0,0,1]
	v_med3_f32 v26, v44, s35, v84
	v_med3_f32 v28, v46, s35, v84
	v_cvt_pk_fp8_f32 v96, v26, v28
	ds_read2_b32 v[52:53], v85 offset0:140 offset1:156
	ds_read2_b32 v[54:55], v85 offset0:173 offset1:189
	ds_read2_b32 v[56:57], v85 offset0:206 offset1:222
	s_waitcnt lgkmcnt(4)
	v_mul_f32_e32 v48, 0x42800000, v48
	s_waitcnt lgkmcnt(3)
	v_mul_f32_e32 v24, 0x42800000, v50
	v_med3_f32 v26, v48, s35, v84
	v_med3_f32 v24, v24, s35, v84
	ds_read2_b32 v[58:59], v85 offset0:239 offset1:255
	v_cvt_pk_fp8_f32 v96, v26, v24 op_sel:[0,0,1]
	s_waitcnt lgkmcnt(3)
	v_mul_f32_e32 v24, 0x42800000, v52
	s_waitcnt lgkmcnt(2)
	v_mul_f32_e32 v26, 0x42800000, v54
	v_med3_f32 v24, v24, s35, v84
	v_med3_f32 v26, v26, s35, v84
	v_cvt_pk_fp8_f32 v97, v24, v26
	s_waitcnt lgkmcnt(1)
	v_mul_f32_e32 v28, 0x42800000, v56
	s_waitcnt lgkmcnt(0)
	v_mul_f32_e32 v24, 0x42800000, v58
	v_med3_f32 v26, v28, s35, v84
	v_med3_f32 v24, v24, s35, v84
	v_cvt_pk_fp8_f32 v97, v26, v24 op_sel:[0,0,1]
	v_or_b32_e32 v24, s7, v63
	v_lshlrev_b32_e32 v60, 12, v24
	v_mul_f32_e32 v24, 0x42800000, v25
	v_mul_f32_e32 v25, 0x42800000, v27
	v_med3_f32 v27, v24, s35, v84
	v_med3_f32 v25, v25, s35, v84
	v_mov_b32_e32 v24, v3
	v_cvt_pk_fp8_f32 v24, v27, v25
	v_mul_f32_e32 v26, 0x42800000, v29
	v_mul_f32_e32 v25, 0x42800000, v31
	v_med3_f32 v26, v26, s35, v84
	v_med3_f32 v25, v25, s35, v84
	v_cvt_pk_fp8_f32 v24, v26, v25 op_sel:[0,0,1]
	v_mul_f32_e32 v25, 0x42800000, v37
	v_mul_f32_e32 v26, 0x42800000, v39
	v_med3_f32 v28, v25, s35, v84
	v_med3_f32 v26, v26, s35, v84
	v_mov_b32_e32 v25, v3
	v_cvt_pk_fp8_f32 v25, v28, v26
	v_mul_f32_e32 v27, 0x42800000, v41
	v_mul_f32_e32 v26, 0x42800000, v43
	v_med3_f32 v27, v27, s35, v84
	v_med3_f32 v26, v26, s35, v84
	v_cvt_pk_fp8_f32 v25, v27, v26 op_sel:[0,0,1]
	v_mul_f32_e32 v26, 0x42800000, v45
	v_mul_f32_e32 v27, 0x42800000, v47
	v_med3_f32 v29, v26, s35, v84
	v_med3_f32 v27, v27, s35, v84
	v_mov_b32_e32 v26, v3
	v_cvt_pk_fp8_f32 v26, v29, v27
	v_mul_f32_e32 v28, 0x42800000, v49
	v_mul_f32_e32 v27, 0x42800000, v51
	v_med3_f32 v28, v28, s35, v84
	v_med3_f32 v27, v27, s35, v84
	v_cvt_pk_fp8_f32 v26, v28, v27 op_sel:[0,0,1]
	v_mul_f32_e32 v27, 0x42800000, v53
	v_mul_f32_e32 v28, 0x42800000, v55
	v_med3_f32 v30, v27, s35, v84
	v_med3_f32 v28, v28, s35, v84
	v_mov_b32_e32 v27, v3
	v_cvt_pk_fp8_f32 v27, v30, v28
	v_mul_f32_e32 v29, 0x42800000, v57
	v_mul_f32_e32 v28, 0x42800000, v59
	v_med3_f32 v29, v29, s35, v84
	v_med3_f32 v28, v28, s35, v84
	v_cvt_pk_fp8_f32 v27, v29, v28 op_sel:[0,0,1]
	v_or_b32_e32 v28, s7, v65
	v_lshlrev_b32_e32 v28, 12, v28
	v_mov_b32_e32 v29, v3
	v_lshl_add_u64 v[60:61], v[32:33], 0, v[60:61]
	v_lshl_add_u64 v[28:29], v[32:33], 0, v[28:29]
	global_store_dwordx4 v[60:61], v[94:97], off
	global_store_dwordx4 v[28:29], v[24:27], off
	s_waitcnt lgkmcnt(0)

.LBB0_119:
	s_andn2_b64 vcc, exec, s[0:1]
	s_cbranch_vccnz .LBB0_121
	s_add_i32 s0, s3, 0x3e9600
	s_lshr_b32 s0, s0, 6
	s_mulk_i32 s0, 0x120
	s_and_b32 s1, s3, 63
	s_add_i32 s0, s0, s1
	s_add_i32 s0, s0, 64
	s_and_b32 s1, s0, 0xffff
	s_mul_i32 s1, s1, 0xe38f
	s_lshr_b32 s1, s1, 24
	s_mul_i32 s7, s1, 0x120
	s_sub_i32 s0, s0, s7
	v_lshl_or_b32 v24, s1, 6, v35
	s_lshl_b32 s0, s0, 5
	v_mul_u32_u24_e32 v24, 0x2400, v24
	v_readlane_b32 s36, v247, 22
	s_and_b32 s0, s0, 0xffe0
	v_lshlrev_b32_e32 v24, 2, v24
	v_mov_b32_e32 v25, v3
	v_readlane_b32 s38, v247, 24
	v_readlane_b32 s39, v247, 25
	s_lshl_b32 s10, s0, 2
	s_addk_i32 s0, 0xf800
	v_lshl_add_u64 v[24:25], s[38:39], 0, v[24:25]
	v_lshl_add_u64 v[24:25], v[24:25], 0, s[10:11]
	v_lshl_add_u64 v[32:33], v[24:25], 0, v[2:3]
	v_add_co_u32_e32 v28, vcc, s69, v32
	s_lshl_b32 s10, s1, 7
	s_nop 0
	v_addc_co_u32_e32 v29, vcc, 0, v33, vcc
	v_add_co_u32_e32 v36, vcc, s70, v32
	s_nop 0
	v_addc_co_u32_e32 v37, vcc, 0, v33, vcc
	v_add_co_u32_e32 v40, vcc, s71, v32
	v_readlane_b32 s37, v247, 23
	s_nop 0
	v_addc_co_u32_e32 v41, vcc, 0, v33, vcc
	v_add_co_u32_e32 v44, vcc, s93, v32
	s_nop 0
	v_addc_co_u32_e32 v45, vcc, 0, v33, vcc
	v_add_co_u32_e32 v48, vcc, s94, v32
	v_readlane_b32 s40, v247, 26
	s_nop 0
	v_addc_co_u32_e32 v49, vcc, 0, v33, vcc
	s_nop 0
	v_add_co_u32_e32 v52, vcc, s95, v32
	v_readlane_b32 s41, v247, 27
	s_nop 0
	v_addc_co_u32_e32 v53, vcc, 0, v33, vcc
	v_add_co_u32_e32 v32, vcc, s60, v32
	v_readlane_b32 s42, v247, 28
	s_nop 0
	v_addc_co_u32_e32 v33, vcc, 0, v33, vcc
	v_lshl_add_u64 v[32:33], v[14:15], 0, s[10:11]
	v_readlane_b32 s43, v247, 29
	v_readlane_b32 s44, v247, 30
	v_readlane_b32 s45, v247, 31
	v_readlane_b32 s46, v247, 32
	v_readlane_b32 s47, v247, 33
	v_readlane_b32 s48, v247, 34
	v_readlane_b32 s49, v247, 35
	v_readlane_b32 s50, v247, 36
	v_readlane_b32 s51, v247, 37
	s_waitcnt lgkmcnt(0)
	ds_read2_b32 v[28:29], v66 offset0:33 offset1:41
	ds_read2_b32 v[30:31], v66 offset1:8
	ds_read2_b32 v[36:37], v66 offset0:66 offset1:74
	ds_read2_b32 v[38:39], v66 offset0:99 offset1:107
	ds_read2_b32 v[40:41], v66 offset0:132 offset1:140
	ds_read2_b32 v[42:43], v66 offset0:165 offset1:173
	ds_read2_b32 v[44:45], v66 offset0:198 offset1:206
	ds_read2_b32 v[46:47], v66 offset0:231 offset1:239
	s_waitcnt lgkmcnt(7)
	v_bfe_u32 v25, v28, 16, 1
	s_waitcnt lgkmcnt(3)
	v_bfe_u32 v48, v40, 16, 1
	v_bfe_u32 v24, v30, 16, 1
	v_bfe_u32 v26, v36, 16, 1
	s_waitcnt lgkmcnt(2)
	v_bfe_u32 v49, v42, 16, 1
	s_waitcnt lgkmcnt(1)
	v_bfe_u32 v50, v44, 16, 1
	v_add3_u32 v25, v28, v25, s67
	v_add3_u32 v28, v40, v48, s67
	v_or_b32_e32 v48, s0, v35
	v_bfe_u32 v27, v38, 16, 1
	s_waitcnt lgkmcnt(0)
	v_bfe_u32 v51, v46, 16, 1
	v_add3_u32 v24, v30, v24, s67
	v_add3_u32 v26, v36, v26, s67
	v_add3_u32 v30, v42, v49, s67
	v_add3_u32 v36, v44, v50, s67
	v_ashrrev_i32_e32 v49, 31, v48
	v_add3_u32 v27, v38, v27, s67
	v_add3_u32 v38, v46, v51, s67
	v_lshrrev_b32_e32 v24, 16, v24
	v_lshrrev_b32_e32 v26, 16, v26
	v_lshrrev_b32_e32 v28, 16, v28
	v_lshrrev_b32_e32 v36, 16, v36
	v_lshlrev_b64 v[48:49], 13, v[48:49]
	v_and_or_b32 v24, v25, s68, v24
	v_and_or_b32 v25, v27, s68, v26
	v_and_or_b32 v26, v30, s68, v28
	v_and_or_b32 v27, v38, s68, v36
	v_lshl_add_u64 v[48:49], v[32:33], 0, v[48:49]
	global_store_dwordx4 v[48:49], v[24:27], off
	v_bfe_u32 v28, v47, 16, 1
	v_add3_u32 v28, v47, v28, s67
	v_bfe_u32 v24, v31, 16, 1
	v_add3_u32 v24, v31, v24, s67
	v_bfe_u32 v25, v29, 16, 1
	v_lshrrev_b32_e32 v24, 16, v24
	v_add3_u32 v25, v29, v25, s67
	v_and_or_b32 v24, v25, s68, v24
	v_bfe_u32 v25, v37, 16, 1
	v_add3_u32 v25, v37, v25, s67
	v_bfe_u32 v26, v39, 16, 1
	v_lshrrev_b32_e32 v25, 16, v25
	v_add3_u32 v26, v39, v26, s67
	v_and_or_b32 v25, v26, s68, v25
	v_bfe_u32 v26, v41, 16, 1
	v_add3_u32 v26, v41, v26, s67
	v_bfe_u32 v27, v43, 16, 1
	v_lshrrev_b32_e32 v26, 16, v26
	v_add3_u32 v27, v43, v27, s67
	v_and_or_b32 v26, v27, s68, v26
	v_bfe_u32 v27, v45, 16, 1
	v_add3_u32 v27, v45, v27, s67
	v_lshrrev_b32_e32 v27, 16, v27
	v_and_or_b32 v27, v28, s68, v27
	v_or_b32_e32 v28, s0, v67
	v_ashrrev_i32_e32 v29, 31, v28
	v_lshlrev_b64 v[28:29], 13, v[28:29]
	ds_read2_b32 v[30:31], v66 offset0:16 offset1:24
	v_lshl_add_u64 v[28:29], v[32:33], 0, v[28:29]
	global_store_dwordx4 v[28:29], v[24:27], off
	ds_read2_b32 v[28:29], v66 offset0:49 offset1:57
	ds_read2_b32 v[36:37], v66 offset0:82 offset1:90
	ds_read2_b32 v[38:39], v66 offset0:115 offset1:123
	s_waitcnt lgkmcnt(3)
	v_bfe_u32 v24, v30, 16, 1
	v_add3_u32 v24, v30, v24, s67
	s_waitcnt lgkmcnt(2)
	v_bfe_u32 v25, v28, 16, 1
	ds_read2_b32 v[40:41], v66 offset0:148 offset1:156
	v_lshrrev_b32_e32 v24, 16, v24
	v_add3_u32 v25, v28, v25, s67
	ds_read2_b32 v[42:43], v66 offset0:181 offset1:189
	v_and_or_b32 v24, v25, s68, v24
	s_waitcnt lgkmcnt(3)
	v_bfe_u32 v25, v36, 16, 1
	v_add3_u32 v25, v36, v25, s67
	s_waitcnt lgkmcnt(2)
	v_bfe_u32 v26, v38, 16, 1
	ds_read2_b32 v[44:45], v66 offset0:214 offset1:222
	v_lshrrev_b32_e32 v25, 16, v25
	v_add3_u32 v26, v38, v26, s67
	ds_read2_b32 v[46:47], v66 offset0:247 offset1:255
	v_and_or_b32 v25, v26, s68, v25
	s_waitcnt lgkmcnt(3)
	v_bfe_u32 v26, v40, 16, 1
	v_add3_u32 v26, v40, v26, s67
	s_waitcnt lgkmcnt(2)
	v_bfe_u32 v27, v42, 16, 1
	v_lshrrev_b32_e32 v26, 16, v26
	v_add3_u32 v27, v42, v27, s67
	v_and_or_b32 v26, v27, s68, v26
	s_waitcnt lgkmcnt(1)
	v_bfe_u32 v27, v44, 16, 1
	v_or_b32_e32 v48, s0, v68
	v_add3_u32 v27, v44, v27, s67
	s_waitcnt lgkmcnt(0)
	v_bfe_u32 v28, v46, 16, 1
	v_ashrrev_i32_e32 v49, 31, v48
	v_lshrrev_b32_e32 v27, 16, v27
	v_add3_u32 v28, v46, v28, s67
	v_lshlrev_b64 v[48:49], 13, v[48:49]
	v_and_or_b32 v27, v28, s68, v27
	v_lshl_add_u64 v[48:49], v[32:33], 0, v[48:49]
	global_store_dwordx4 v[48:49], v[24:27], off
	v_bfe_u32 v28, v47, 16, 1
	v_add3_u32 v28, v47, v28, s67
	v_bfe_u32 v24, v31, 16, 1
	v_add3_u32 v24, v31, v24, s67
	v_bfe_u32 v25, v29, 16, 1
	v_lshrrev_b32_e32 v24, 16, v24
	v_add3_u32 v25, v29, v25, s67
	v_and_or_b32 v24, v25, s68, v24
	v_bfe_u32 v25, v37, 16, 1
	v_add3_u32 v25, v37, v25, s67
	v_bfe_u32 v26, v39, 16, 1
	v_lshrrev_b32_e32 v25, 16, v25
	v_add3_u32 v26, v39, v26, s67
	v_and_or_b32 v25, v26, s68, v25
	v_bfe_u32 v26, v41, 16, 1
	v_add3_u32 v26, v41, v26, s67
	v_bfe_u32 v27, v43, 16, 1
	v_lshrrev_b32_e32 v26, 16, v26
	v_add3_u32 v27, v43, v27, s67
	v_and_or_b32 v26, v27, s68, v26
	v_bfe_u32 v27, v45, 16, 1
	v_add3_u32 v27, v45, v27, s67
	v_lshrrev_b32_e32 v27, 16, v27
	v_and_or_b32 v27, v28, s68, v27
	v_or_b32_e32 v28, s0, v69
	v_ashrrev_i32_e32 v29, 31, v28
	v_lshlrev_b64 v[28:29], 13, v[28:29]
	v_lshl_add_u64 v[28:29], v[32:33], 0, v[28:29]
	global_store_dwordx4 v[28:29], v[24:27], off
	s_waitcnt lgkmcnt(0)

.LBB0_122:
	s_andn2_b64 vcc, exec, s[0:1]
	s_cbranch_vccnz .LBB0_124
	s_add_i32 s0, s3, 0xb600
	s_lshr_b32 s0, s0, 1
	s_and_b32 s0, s0, 0x7fc0
	v_or_b32_e32 v24, s0, v35
	v_readlane_b32 s36, v247, 22
	s_and_b32 s1, s14, 0xfe0
	v_lshlrev_b32_e32 v24, 14, v24
	v_mov_b32_e32 v25, v3
	v_readlane_b32 s48, v247, 34
	v_readlane_b32 s49, v247, 35
	s_lshl_b32 s10, s1, 2
	v_readlane_b32 s12, v246, 3
	v_lshl_add_u64 v[24:25], s[48:49], 0, v[24:25]
	v_lshl_add_u64 v[24:25], v[24:25], 0, s[10:11]
	v_lshl_add_u64 v[32:33], v[24:25], 0, v[2:3]
	v_add_co_u32_e32 v28, vcc, s18, v32
	v_readlane_b32 s13, v246, 4
	s_nop 0
	v_addc_co_u32_e32 v29, vcc, 0, v33, vcc
	v_add_co_u32_e32 v36, vcc, s19, v32
	s_nop 0
	v_addc_co_u32_e32 v37, vcc, 0, v33, vcc
	v_add_co_u32_e32 v40, vcc, s20, v32
	v_or_b32_e32 v87, s1, v65
	s_nop 0
	v_addc_co_u32_e32 v41, vcc, 0, v33, vcc
	v_add_co_u32_e32 v44, vcc, s21, v32
	s_nop 0
	v_addc_co_u32_e32 v45, vcc, 0, v33, vcc
	v_add_co_u32_e32 v48, vcc, s30, v32
	v_readlane_b32 s37, v247, 23
	s_nop 0
	v_addc_co_u32_e32 v49, vcc, 0, v33, vcc
	s_nop 0
	v_add_co_u32_e32 v52, vcc, s31, v32
	v_readlane_b32 s38, v247, 24
	s_nop 0
	v_addc_co_u32_e32 v53, vcc, 0, v33, vcc
	v_add_co_u32_e32 v32, vcc, s34, v32
	v_readlane_b32 s39, v247, 25
	s_nop 0
	v_addc_co_u32_e32 v33, vcc, 0, v33, vcc
	v_or_b32_e32 v32, s1, v63
	v_lshlrev_b32_e32 v33, 2, v32
	s_mov_b32 s1, s11
	v_readlane_b32 s40, v247, 26
	v_readlane_b32 s41, v247, 27
	v_readlane_b32 s42, v247, 28
	v_readlane_b32 s43, v247, 29
	v_readlane_b32 s44, v247, 30
	v_readlane_b32 s45, v247, 31
	v_readlane_b32 s46, v247, 32
	v_readlane_b32 s47, v247, 33
	v_readlane_b32 s50, v247, 36
	v_readlane_b32 s51, v247, 37
	s_waitcnt lgkmcnt(0)
	v_mov_b32_e32 v44, v234
	v_lshlrev_b32_e32 v24, 2, v87
	v_mov_b32_e32 v91, v235
	v_lshl_add_u64 v[24:25], v[16:17], 0, s[0:1]
	v_mov_b32_e32 v27, v3
	v_lshlrev_b32_e32 v26, 12, v32
	v_lshl_add_u64 v[48:49], v[24:25], 0, v[26:27]
	ds_read2_b32 v[50:51], v64 offset1:16
	ds_read2_b32 v[52:53], v64 offset0:33 offset1:49
	ds_read2_b32 v[54:55], v64 offset0:66 offset1:82
	ds_read2_b32 v[56:57], v64 offset0:99 offset1:115
	ds_read2_b32 v[58:59], v64 offset0:132 offset1:148
	ds_read2_b32 v[60:61], v64 offset0:165 offset1:181
	ds_read2_b32 v[88:89], v64 offset0:198 offset1:214
	ds_read2_b32 v[94:95], v64 offset0:231 offset1:247
	ds_read2_b32 v[36:37], v85 offset0:8 offset1:24
	ds_read2_b32 v[38:39], v85 offset0:41 offset1:57
	ds_read2_b32 v[40:41], v85 offset0:74 offset1:90
	ds_read2_b32 v[42:43], v85 offset0:107 offset1:123
	ds_read2_b32 v[26:27], v85 offset0:140 offset1:156
	ds_read2_b32 v[28:29], v85 offset0:173 offset1:189
	ds_read2_b32 v[30:31], v85 offset0:206 offset1:222
	ds_read2_b32 v[32:33], v85 offset0:239 offset1:255
	v_div_scale_f32 v45, s[0:1], v44, v44, s61
	v_rcp_f32_e32 v47, v45
	v_div_scale_f32 v46, vcc, s61, v44, s61
	v_div_scale_f32 v93, s[0:1], v91, v91, s61
	v_fma_f32 v98, -v45, v47, 1.0
	v_fmac_f32_e32 v47, v98, v47
	v_mul_f32_e32 v98, v46, v47
	v_fma_f32 v100, -v45, v98, v46
	v_fmac_f32_e32 v98, v100, v47
	v_fma_f32 v45, -v45, v98, v46
	v_div_fmas_f32 v45, v45, v47, v98
	v_div_fixup_f32 v45, v45, v44, s61
	v_cmp_lt_f32_e32 vcc, 0, v44
	v_rcp_f32_e32 v96, v93
	v_div_scale_f32 v97, s[0:1], s61, v91, s61
	v_cndmask_b32_e32 v44, 0, v45, vcc
	s_waitcnt lgkmcnt(14)
	v_mul_f32_e32 v45, v50, v44
	v_mul_f32_e32 v46, v52, v44
	s_waitcnt lgkmcnt(2)
	v_mul_f32_e32 v28, v44, v28
	v_mul_f32_e32 v47, v44, v54
	v_mul_f32_e32 v50, v44, v56
	v_mul_f32_e32 v52, v44, v58
	v_mul_f32_e32 v54, v44, v60
	v_mul_f32_e32 v56, v44, v88
	v_mul_f32_e32 v58, v44, v94
	v_mul_f32_e32 v36, v44, v36
	v_mul_f32_e32 v38, v44, v38
	v_mul_f32_e32 v40, v44, v40
	v_mul_f32_e32 v42, v44, v42
	v_mul_f32_e32 v26, v44, v26
	s_waitcnt lgkmcnt(1)
	v_mul_f32_e32 v30, v44, v30
	s_waitcnt lgkmcnt(0)
	v_mul_f32_e32 v32, v44, v32
	v_med3_f32 v44, v45, s62, v86
	v_med3_f32 v45, v46, s62, v86
	v_med3_f32 v28, v28, s62, v86
	v_med3_f32 v46, v47, s62, v86
	v_med3_f32 v26, v26, s62, v86
	v_med3_f32 v30, v30, s62, v86
	v_rndne_f32_e32 v45, v45
	v_rndne_f32_e32 v28, v28
	v_med3_f32 v47, v50, s62, v86
	v_med3_f32 v32, v32, s62, v86
	v_rndne_f32_e32 v44, v44
	v_rndne_f32_e32 v46, v46
	v_rndne_f32_e32 v26, v26
	v_rndne_f32_e32 v30, v30
	v_cvt_i32_f32_e32 v45, v45
	v_cvt_i32_f32_e32 v28, v28
	v_fma_f32 v99, -v93, v96, 1.0
	v_rndne_f32_e32 v47, v47
	v_rndne_f32_e32 v32, v32
	v_cvt_i32_f32_e32 v44, v44
	v_cvt_i32_f32_sdwa v46, v46 dst_sel:WORD_1 dst_unused:UNUSED_PAD src0_sel:DWORD
	v_cvt_i32_f32_e32 v26, v26
	v_cvt_i32_f32_sdwa v30, v30 dst_sel:WORD_1 dst_unused:UNUSED_PAD src0_sel:DWORD
	v_fmac_f32_e32 v96, v99, v96
	v_cvt_i32_f32_sdwa v47, v47 dst_sel:BYTE_3 dst_unused:UNUSED_PAD src0_sel:DWORD
	v_cvt_i32_f32_sdwa v32, v32 dst_sel:BYTE_3 dst_unused:UNUSED_PAD src0_sel:DWORD
	v_mul_f32_e32 v99, v97, v96
	v_fma_f32 v101, -v93, v99, v97
	v_med3_f32 v38, v38, s62, v86
	v_lshlrev_b32_e32 v45, 8, v45
	v_lshlrev_b32_e32 v28, 8, v28
	v_med3_f32 v36, v36, s62, v86
	v_med3_f32 v40, v40, s62, v86
	v_rndne_f32_e32 v38, v38
	v_and_b32_e32 v46, 0xff0000, v46
	v_and_b32_e32 v30, 0xff0000, v30
	v_perm_b32 v44, v45, v44, s63
	v_perm_b32 v26, v28, v26, s63
	v_fmac_f32_e32 v99, v101, v96
	v_med3_f32 v42, v42, s62, v86
	v_rndne_f32_e32 v36, v36
	v_rndne_f32_e32 v40, v40
	v_cvt_i32_f32_e32 v38, v38
	v_or3_b32 v44, v44, v46, v47
	v_or3_b32 v47, v26, v30, v32
	v_fma_f32 v26, -v93, v99, v97
	s_mov_b64 vcc, s[0:1]
	v_rndne_f32_e32 v42, v42
	v_cvt_i32_f32_e32 v36, v36
	v_cvt_i32_f32_sdwa v40, v40 dst_sel:WORD_1 dst_unused:UNUSED_PAD src0_sel:DWORD
	v_div_fmas_f32 v26, v26, v96, v99
	v_cvt_i32_f32_sdwa v42, v42 dst_sel:BYTE_3 dst_unused:UNUSED_PAD src0_sel:DWORD
	v_div_fixup_f32 v26, v26, v91, s61
	v_cmp_lt_f32_e32 vcc, 0, v91
	v_med3_f32 v50, v52, s62, v86
	v_med3_f32 v52, v54, s62, v86
	v_cndmask_b32_e32 v26, 0, v26, vcc
	v_lshlrev_b32_e32 v38, 8, v38
	v_mul_f32_e32 v30, v53, v26
	v_med3_f32 v54, v56, s62, v86
	v_rndne_f32_e32 v52, v52
	v_and_b32_e32 v40, 0xff0000, v40
	v_perm_b32 v36, v38, v36, s63
	v_mul_f32_e32 v28, v51, v26
	v_mul_f32_e32 v32, v26, v55
	v_med3_f32 v30, v30, s62, v86
	v_med3_f32 v56, v58, s62, v86
	v_rndne_f32_e32 v50, v50
	v_rndne_f32_e32 v54, v54
	v_cvt_i32_f32_e32 v52, v52
	v_or3_b32 v46, v36, v40, v42
	v_mul_f32_e32 v36, v26, v57
	v_med3_f32 v28, v28, s62, v86
	v_rndne_f32_e32 v30, v30
	v_med3_f32 v32, v32, s62, v86
	v_rndne_f32_e32 v56, v56
	v_cvt_i32_f32_e32 v50, v50
	v_cvt_i32_f32_sdwa v54, v54 dst_sel:WORD_1 dst_unused:UNUSED_PAD src0_sel:DWORD
	v_rndne_f32_e32 v28, v28
	v_cvt_i32_f32_e32 v30, v30
	v_rndne_f32_e32 v32, v32
	v_med3_f32 v36, v36, s62, v86
	v_cvt_i32_f32_sdwa v56, v56 dst_sel:BYTE_3 dst_unused:UNUSED_PAD src0_sel:DWORD
	v_cvt_i32_f32_e32 v28, v28
	v_cvt_i32_f32_sdwa v32, v32 dst_sel:WORD_1 dst_unused:UNUSED_PAD src0_sel:DWORD
	v_rndne_f32_e32 v36, v36
	v_cvt_i32_f32_sdwa v36, v36 dst_sel:BYTE_3 dst_unused:UNUSED_PAD src0_sel:DWORD
	v_lshlrev_b32_e32 v52, 8, v52
	v_and_b32_e32 v54, 0xff0000, v54
	v_perm_b32 v45, v52, v50, s63
	v_lshlrev_b32_e32 v30, 8, v30
	v_or3_b32 v45, v45, v54, v56
	v_perm_b32 v28, v30, v28, s63
	v_and_b32_e32 v30, 0xff0000, v32
	global_store_dwordx4 v[48:49], v[44:47], off
	v_mul_f32_e32 v32, v26, v89
	v_med3_f32 v32, v32, s62, v86
	v_or3_b32 v44, v28, v30, v36
	v_mul_f32_e32 v30, v26, v61
	v_mul_f32_e32 v28, v26, v59
	v_med3_f32 v30, v30, s62, v86
	v_mul_f32_e32 v36, v26, v95
	v_med3_f32 v28, v28, s62, v86
	v_rndne_f32_e32 v30, v30
	v_rndne_f32_e32 v28, v28
	v_cvt_i32_f32_e32 v30, v30
	v_rndne_f32_e32 v32, v32
	v_med3_f32 v36, v36, s62, v86
	v_cvt_i32_f32_e32 v28, v28
	v_cvt_i32_f32_sdwa v32, v32 dst_sel:WORD_1 dst_unused:UNUSED_PAD src0_sel:DWORD
	v_rndne_f32_e32 v36, v36
	v_cvt_i32_f32_sdwa v36, v36 dst_sel:BYTE_3 dst_unused:UNUSED_PAD src0_sel:DWORD
	v_lshlrev_b32_e32 v30, 8, v30
	v_perm_b32 v28, v30, v28, s63
	v_and_b32_e32 v30, 0xff0000, v32
	v_or3_b32 v45, v28, v30, v36
	v_mul_f32_e32 v30, v26, v39
	v_mul_f32_e32 v28, v26, v37
	v_mul_f32_e32 v32, v26, v41
	v_med3_f32 v30, v30, s62, v86
	v_mul_f32_e32 v36, v26, v43
	v_med3_f32 v28, v28, s62, v86
	v_rndne_f32_e32 v30, v30
	v_med3_f32 v32, v32, s62, v86
	v_rndne_f32_e32 v28, v28
	v_cvt_i32_f32_e32 v30, v30
	v_rndne_f32_e32 v32, v32
	v_med3_f32 v36, v36, s62, v86
	v_cvt_i32_f32_e32 v28, v28
	v_cvt_i32_f32_sdwa v32, v32 dst_sel:WORD_1 dst_unused:UNUSED_PAD src0_sel:DWORD
	v_rndne_f32_e32 v36, v36
	v_cvt_i32_f32_sdwa v36, v36 dst_sel:BYTE_3 dst_unused:UNUSED_PAD src0_sel:DWORD
	v_lshlrev_b32_e32 v30, 8, v30
	v_perm_b32 v28, v30, v28, s63
	v_and_b32_e32 v30, 0xff0000, v32
	v_or3_b32 v46, v28, v30, v36
	v_mul_f32_e32 v28, v26, v29
	v_mul_f32_e32 v27, v26, v27
	v_mul_f32_e32 v29, v26, v31
	v_med3_f32 v28, v28, s62, v86
	v_mul_f32_e32 v26, v26, v33
	v_med3_f32 v27, v27, s62, v86
	v_rndne_f32_e32 v28, v28
	v_med3_f32 v29, v29, s62, v86
	v_rndne_f32_e32 v27, v27
	v_cvt_i32_f32_e32 v28, v28
	v_rndne_f32_e32 v29, v29
	v_med3_f32 v26, v26, s62, v86
	v_cvt_i32_f32_e32 v27, v27
	v_cvt_i32_f32_sdwa v29, v29 dst_sel:WORD_1 dst_unused:UNUSED_PAD src0_sel:DWORD
	v_rndne_f32_e32 v26, v26
	v_cvt_i32_f32_sdwa v26, v26 dst_sel:BYTE_3 dst_unused:UNUSED_PAD src0_sel:DWORD
	v_lshlrev_b32_e32 v28, 8, v28
	v_perm_b32 v27, v28, v27, s63
	v_and_b32_e32 v28, 0xff0000, v29
	v_or3_b32 v47, v27, v28, v26
	v_lshlrev_b32_e32 v26, 12, v87
	v_mov_b32_e32 v27, v3
	v_lshl_add_u64 v[24:25], v[24:25], 0, v[26:27]
	global_store_dwordx4 v[24:25], v[44:47], off
	s_waitcnt lgkmcnt(0)

.LBB0_125:
	s_andn2_b64 vcc, exec, s[0:1]
	s_cbranch_vccnz .LBB0_127
	s_add_i32 s0, s3, 0xfe00
	s_and_b32 s1, s0, 0xffff
	s_mul_i32 s1, s1, 0xe38f
	s_lshr_b32 s1, s1, 24
	s_mul_i32 s7, s1, 0x120
	s_sub_i32 s7, s0, s7
	s_lshl_b32 s0, s1, 6
	v_or_b32_e32 v24, s0, v35
	s_lshl_b32 s1, s7, 5
	v_mul_u32_u24_e32 v24, 0x2400, v24
	v_readlane_b32 s36, v247, 22
	s_and_b32 s1, s1, 0xffe0
	v_lshlrev_b32_e32 v24, 2, v24
	v_mov_b32_e32 v25, v3
	v_readlane_b32 s38, v247, 24
	v_readlane_b32 s39, v247, 25
	s_lshl_b32 s10, s1, 2
	v_or_b32_e32 v87, s1, v65
	v_lshl_add_u64 v[24:25], s[38:39], 0, v[24:25]
	v_lshl_add_u64 v[24:25], v[24:25], 0, s[10:11]
	v_lshl_add_u64 v[32:33], v[24:25], 0, v[2:3]
	v_add_co_u32_e32 v28, vcc, s69, v32
	v_readlane_b32 s37, v247, 23
	s_nop 0
	v_addc_co_u32_e32 v29, vcc, 0, v33, vcc
	v_add_co_u32_e32 v36, vcc, s70, v32
	s_nop 0
	v_addc_co_u32_e32 v37, vcc, 0, v33, vcc
	v_add_co_u32_e32 v40, vcc, s71, v32
	v_readlane_b32 s40, v247, 26
	s_nop 0
	v_addc_co_u32_e32 v41, vcc, 0, v33, vcc
	v_add_co_u32_e32 v44, vcc, s93, v32
	s_nop 0
	v_addc_co_u32_e32 v45, vcc, 0, v33, vcc
	v_add_co_u32_e32 v48, vcc, s94, v32
	v_readlane_b32 s41, v247, 27
	s_nop 0
	v_addc_co_u32_e32 v49, vcc, 0, v33, vcc
	s_nop 0
	v_add_co_u32_e32 v52, vcc, s95, v32
	v_readlane_b32 s42, v247, 28
	s_nop 0
	v_addc_co_u32_e32 v53, vcc, 0, v33, vcc
	v_add_co_u32_e32 v32, vcc, s60, v32
	v_readlane_b32 s43, v247, 29
	s_nop 0
	v_addc_co_u32_e32 v33, vcc, 0, v33, vcc
	v_or_b32_e32 v32, s1, v63
	v_lshlrev_b32_e32 v33, 2, v32
	s_mov_b32 s1, s11
	v_readlane_b32 s44, v247, 30
	v_readlane_b32 s45, v247, 31
	v_readlane_b32 s46, v247, 32
	v_readlane_b32 s47, v247, 33
	v_readlane_b32 s48, v247, 34
	v_readlane_b32 s49, v247, 35
	v_readlane_b32 s50, v247, 36
	v_readlane_b32 s51, v247, 37
	s_waitcnt lgkmcnt(0)
	v_mov_b32_e32 v26, v234
	v_lshlrev_b32_e32 v24, 2, v87
	v_mov_b32_e32 v91, v235
	v_mov_b32_e32 v25, v3
	v_lshl_add_u64 v[28:29], v[18:19], 0, s[0:1]
	v_lshlrev_b32_e32 v24, 12, v32
	v_lshl_add_u64 v[30:31], v[28:29], 0, v[24:25]
	ds_read2_b32 v[32:33], v64 offset1:16
	ds_read2_b32 v[36:37], v64 offset0:33 offset1:49
	ds_read2_b32 v[38:39], v64 offset0:66 offset1:82
	ds_read2_b32 v[40:41], v64 offset0:99 offset1:115
	ds_read2_b32 v[42:43], v64 offset0:132 offset1:148
	ds_read2_b32 v[44:45], v64 offset0:165 offset1:181
	ds_read2_b32 v[46:47], v64 offset0:198 offset1:214
	ds_read2_b32 v[48:49], v64 offset0:231 offset1:247
	ds_read2_b32 v[50:51], v85 offset0:8 offset1:24
	ds_read2_b32 v[52:53], v85 offset0:41 offset1:57
	ds_read2_b32 v[54:55], v85 offset0:74 offset1:90
	ds_read2_b32 v[56:57], v85 offset0:107 offset1:123
	ds_read2_b32 v[58:59], v85 offset0:140 offset1:156
	ds_read2_b32 v[60:61], v85 offset0:173 offset1:189
	ds_read2_b32 v[88:89], v85 offset0:206 offset1:222
	ds_read2_b32 v[94:95], v85 offset0:239 offset1:255
	v_div_scale_f32 v24, s[0:1], v26, v26, s61
	v_rcp_f32_e32 v25, v24
	v_div_scale_f32 v93, s[0:1], v91, v91, s61
	v_rcp_f32_e32 v96, v93
	v_fma_f32 v97, -v24, v25, 1.0
	v_div_scale_f32 v27, vcc, s61, v26, s61
	v_fmac_f32_e32 v25, v97, v25
	v_fma_f32 v98, -v93, v96, 1.0
	v_mul_f32_e32 v97, v27, v25
	v_fmac_f32_e32 v96, v98, v96
	v_fma_f32 v98, -v24, v97, v27
	v_fmac_f32_e32 v97, v98, v25
	v_fma_f32 v24, -v24, v97, v27
	v_div_fmas_f32 v24, v24, v25, v97
	v_div_fixup_f32 v24, v24, v26, s61
	v_cmp_lt_f32_e32 vcc, 0, v26
	s_nop 1
	v_cndmask_b32_e32 v24, 0, v24, vcc
	s_waitcnt lgkmcnt(14)
	v_mul_f32_e32 v25, v32, v24
	v_mul_f32_e32 v26, v36, v24
	s_waitcnt lgkmcnt(13)
	v_mul_f32_e32 v27, v24, v38
	s_waitcnt lgkmcnt(12)
	v_mul_f32_e32 v32, v24, v40
	s_waitcnt lgkmcnt(11)
	v_mul_f32_e32 v36, v24, v42
	s_waitcnt lgkmcnt(10)
	v_mul_f32_e32 v38, v24, v44
	s_waitcnt lgkmcnt(9)
	v_mul_f32_e32 v40, v24, v46
	s_waitcnt lgkmcnt(8)
	v_mul_f32_e32 v42, v24, v48
	s_waitcnt lgkmcnt(6)
	v_mul_f32_e32 v46, v24, v52
	s_waitcnt lgkmcnt(5)
	v_mul_f32_e32 v48, v24, v54
	s_waitcnt lgkmcnt(2)
	v_mul_f32_e32 v54, v24, v60
	v_mul_f32_e32 v44, v24, v50
	v_mul_f32_e32 v50, v24, v56
	v_mul_f32_e32 v52, v24, v58
	s_waitcnt lgkmcnt(1)
	v_mul_f32_e32 v56, v24, v88
	v_med3_f32 v26, v26, s62, v86
	v_med3_f32 v27, v27, s62, v86
	v_med3_f32 v38, v38, s62, v86
	v_med3_f32 v40, v40, s62, v86
	v_med3_f32 v46, v46, s62, v86
	v_med3_f32 v48, v48, s62, v86
	v_med3_f32 v54, v54, s62, v86
	s_waitcnt lgkmcnt(0)
	v_mul_f32_e32 v24, v24, v94
	v_med3_f32 v25, v25, s62, v86
	v_med3_f32 v36, v36, s62, v86
	v_med3_f32 v44, v44, s62, v86
	v_med3_f32 v52, v52, s62, v86
	v_med3_f32 v56, v56, s62, v86
	v_rndne_f32_e32 v26, v26
	v_rndne_f32_e32 v27, v27
	v_rndne_f32_e32 v38, v38
	v_rndne_f32_e32 v40, v40
	v_rndne_f32_e32 v46, v46
	v_rndne_f32_e32 v48, v48
	v_rndne_f32_e32 v54, v54
	v_med3_f32 v32, v32, s62, v86
	v_med3_f32 v42, v42, s62, v86
	v_med3_f32 v50, v50, s62, v86
	v_med3_f32 v24, v24, s62, v86
	v_rndne_f32_e32 v25, v25
	v_rndne_f32_e32 v36, v36
	v_rndne_f32_e32 v44, v44
	v_rndne_f32_e32 v52, v52
	v_rndne_f32_e32 v56, v56
	v_cvt_i32_f32_e32 v26, v26
	v_cvt_i32_f32_sdwa v27, v27 dst_sel:WORD_1 dst_unused:UNUSED_PAD src0_sel:DWORD
	v_cvt_i32_f32_e32 v38, v38
	v_cvt_i32_f32_sdwa v40, v40 dst_sel:WORD_1 dst_unused:UNUSED_PAD src0_sel:DWORD
	v_cvt_i32_f32_e32 v46, v46
	v_cvt_i32_f32_sdwa v48, v48 dst_sel:WORD_1 dst_unused:UNUSED_PAD src0_sel:DWORD
	v_cvt_i32_f32_e32 v54, v54
	v_rndne_f32_e32 v32, v32
	v_rndne_f32_e32 v42, v42
	v_rndne_f32_e32 v50, v50
	v_rndne_f32_e32 v24, v24
	v_cvt_i32_f32_e32 v25, v25
	v_cvt_i32_f32_e32 v36, v36
	v_cvt_i32_f32_e32 v44, v44
	v_cvt_i32_f32_e32 v52, v52
	v_cvt_i32_f32_sdwa v56, v56 dst_sel:WORD_1 dst_unused:UNUSED_PAD src0_sel:DWORD
	v_cvt_i32_f32_sdwa v32, v32 dst_sel:BYTE_3 dst_unused:UNUSED_PAD src0_sel:DWORD
	v_cvt_i32_f32_sdwa v42, v42 dst_sel:BYTE_3 dst_unused:UNUSED_PAD src0_sel:DWORD
	v_cvt_i32_f32_sdwa v50, v50 dst_sel:BYTE_3 dst_unused:UNUSED_PAD src0_sel:DWORD
	v_cvt_i32_f32_sdwa v58, v24 dst_sel:BYTE_3 dst_unused:UNUSED_PAD src0_sel:DWORD
	v_lshlrev_b32_e32 v24, 8, v26
	v_and_b32_e32 v26, 0xff0000, v27
	v_lshlrev_b32_e32 v27, 8, v38
	v_and_b32_e32 v38, 0xff0000, v40
	v_lshlrev_b32_e32 v40, 8, v46
	v_and_b32_e32 v46, 0xff0000, v48
	v_lshlrev_b32_e32 v48, 8, v54
	v_and_b32_e32 v54, 0xff0000, v56
	v_perm_b32 v24, v24, v25, s63
	v_perm_b32 v25, v27, v36, s63
	v_perm_b32 v27, v40, v44, s63
	v_perm_b32 v36, v48, v52, s63
	v_or3_b32 v24, v24, v26, v32
	v_or3_b32 v25, v25, v38, v42
	v_or3_b32 v26, v27, v46, v50
	v_or3_b32 v27, v36, v54, v58
	global_store_dwordx4 v[30:31], v[24:27], off
	s_nop 1
	v_div_scale_f32 v24, vcc, s61, v91, s61
	v_mul_f32_e32 v25, v24, v96
	v_fma_f32 v26, -v93, v25, v24
	v_fmac_f32_e32 v25, v26, v96
	v_fma_f32 v24, -v93, v25, v24
	v_div_fmas_f32 v24, v24, v96, v25
	v_div_fixup_f32 v24, v24, v91, s61
	v_cmp_lt_f32_e32 vcc, 0, v91
	s_nop 1
	v_cndmask_b32_e32 v27, 0, v24, vcc
	v_mul_f32_e32 v25, v37, v27
	v_mul_f32_e32 v24, v33, v27
	v_mul_f32_e32 v26, v27, v39
	v_med3_f32 v25, v25, s62, v86
	v_mul_f32_e32 v30, v27, v41
	v_med3_f32 v24, v24, s62, v86
	v_rndne_f32_e32 v25, v25
	v_med3_f32 v26, v26, s62, v86
	v_rndne_f32_e32 v24, v24
	v_cvt_i32_f32_e32 v25, v25
	v_rndne_f32_e32 v26, v26
	v_med3_f32 v30, v30, s62, v86
	v_cvt_i32_f32_e32 v24, v24
	v_cvt_i32_f32_sdwa v26, v26 dst_sel:WORD_1 dst_unused:UNUSED_PAD src0_sel:DWORD
	v_rndne_f32_e32 v30, v30
	v_cvt_i32_f32_sdwa v30, v30 dst_sel:BYTE_3 dst_unused:UNUSED_PAD src0_sel:DWORD
	v_lshlrev_b32_e32 v25, 8, v25
	v_perm_b32 v24, v25, v24, s63
	v_and_b32_e32 v25, 0xff0000, v26
	v_mul_f32_e32 v26, v27, v45
	v_or3_b32 v24, v24, v25, v30
	v_mul_f32_e32 v25, v27, v43
	v_mul_f32_e32 v30, v27, v47
	v_med3_f32 v26, v26, s62, v86
	v_mul_f32_e32 v31, v27, v49
	v_med3_f32 v25, v25, s62, v86
	v_rndne_f32_e32 v26, v26
	v_med3_f32 v30, v30, s62, v86
	v_rndne_f32_e32 v25, v25
	v_cvt_i32_f32_e32 v26, v26
	v_rndne_f32_e32 v30, v30
	v_med3_f32 v31, v31, s62, v86
	v_cvt_i32_f32_e32 v25, v25
	v_cvt_i32_f32_sdwa v30, v30 dst_sel:WORD_1 dst_unused:UNUSED_PAD src0_sel:DWORD
	v_rndne_f32_e32 v31, v31
	v_cvt_i32_f32_sdwa v31, v31 dst_sel:BYTE_3 dst_unused:UNUSED_PAD src0_sel:DWORD
	v_lshlrev_b32_e32 v26, 8, v26
	v_perm_b32 v25, v26, v25, s63
	v_and_b32_e32 v26, 0xff0000, v30
	v_mul_f32_e32 v30, v27, v53
	v_or3_b32 v25, v25, v26, v31
	v_mul_f32_e32 v26, v27, v51
	v_mul_f32_e32 v31, v27, v55
	v_med3_f32 v30, v30, s62, v86
	v_mul_f32_e32 v32, v27, v57
	v_med3_f32 v26, v26, s62, v86
	v_rndne_f32_e32 v30, v30
	v_med3_f32 v31, v31, s62, v86
	v_rndne_f32_e32 v26, v26
	v_cvt_i32_f32_e32 v30, v30
	v_rndne_f32_e32 v31, v31
	v_med3_f32 v32, v32, s62, v86
	v_cvt_i32_f32_e32 v26, v26
	v_cvt_i32_f32_sdwa v31, v31 dst_sel:WORD_1 dst_unused:UNUSED_PAD src0_sel:DWORD
	v_rndne_f32_e32 v32, v32
	v_cvt_i32_f32_sdwa v32, v32 dst_sel:BYTE_3 dst_unused:UNUSED_PAD src0_sel:DWORD
	v_lshlrev_b32_e32 v30, 8, v30
	v_perm_b32 v26, v30, v26, s63
	v_and_b32_e32 v30, 0xff0000, v31
	v_mul_f32_e32 v31, v27, v61
	v_or3_b32 v26, v26, v30, v32
	v_mul_f32_e32 v30, v27, v59
	v_mul_f32_e32 v32, v27, v89
	v_med3_f32 v31, v31, s62, v86
	v_mul_f32_e32 v27, v27, v95
	v_med3_f32 v30, v30, s62, v86
	v_rndne_f32_e32 v31, v31
	v_med3_f32 v32, v32, s62, v86
	v_rndne_f32_e32 v30, v30
	v_cvt_i32_f32_e32 v31, v31
	v_rndne_f32_e32 v32, v32
	v_med3_f32 v27, v27, s62, v86
	v_cvt_i32_f32_e32 v30, v30
	v_cvt_i32_f32_sdwa v32, v32 dst_sel:WORD_1 dst_unused:UNUSED_PAD src0_sel:DWORD
	v_rndne_f32_e32 v27, v27
	v_cvt_i32_f32_sdwa v27, v27 dst_sel:BYTE_3 dst_unused:UNUSED_PAD src0_sel:DWORD
	v_lshlrev_b32_e32 v31, 8, v31
	v_perm_b32 v30, v31, v30, s63
	v_and_b32_e32 v31, 0xff0000, v32
	v_or3_b32 v27, v30, v31, v27
	v_lshlrev_b32_e32 v30, 12, v87
	v_mov_b32_e32 v31, v3
	v_lshl_add_u64 v[28:29], v[28:29], 0, v[30:31]
	global_store_dwordx4 v[28:29], v[24:27], off
	s_waitcnt lgkmcnt(0)

.LBB0_128:
	s_andn2_b64 vcc, exec, s[0:1]
	s_cbranch_vccnz .LBB0_130
	s_add_i32 s0, s3, 0x5400
	s_lshr_b32 s0, s0, 1
	s_and_b32 s0, s0, 0x7fc0
	s_lshl_b32 s1, s3, 5
	v_or_b32_e32 v24, s0, v35
	v_readlane_b32 s36, v247, 6
	s_and_b32 s7, s1, 0xfe0
	v_lshlrev_b32_e32 v24, 14, v24
	v_mov_b32_e32 v25, v3
	v_readlane_b32 s50, v247, 20
	v_readlane_b32 s51, v247, 21
	s_lshl_b32 s10, s7, 2
	v_mov_b32_e32 v94, v3
	v_lshl_add_u64 v[24:25], s[50:51], 0, v[24:25]
	v_lshl_add_u64 v[24:25], v[24:25], 0, s[10:11]
	v_lshl_add_u64 v[32:33], v[24:25], 0, v[2:3]
	v_add_co_u32_e32 v28, vcc, s18, v32
	v_mov_b32_e32 v95, v3
	s_nop 0
	v_addc_co_u32_e32 v29, vcc, 0, v33, vcc
	v_add_co_u32_e32 v36, vcc, s19, v32
	s_nop 0
	v_addc_co_u32_e32 v37, vcc, 0, v33, vcc
	v_add_co_u32_e32 v40, vcc, s20, v32
	v_mov_b32_e32 v96, v3
	s_nop 0
	v_addc_co_u32_e32 v41, vcc, 0, v33, vcc
	v_add_co_u32_e32 v44, vcc, s21, v32
	s_nop 0
	v_addc_co_u32_e32 v45, vcc, 0, v33, vcc
	v_add_co_u32_e32 v48, vcc, s30, v32
	v_mov_b32_e32 v97, v3
	s_nop 0
	v_addc_co_u32_e32 v49, vcc, 0, v33, vcc
	s_nop 0
	v_add_co_u32_e32 v52, vcc, s31, v32
	s_mov_b32 s1, s11
	s_nop 0
	v_addc_co_u32_e32 v53, vcc, 0, v33, vcc
	v_add_co_u32_e32 v32, vcc, s34, v32
	v_mov_b32_e32 v61, v3
	s_nop 0
	v_addc_co_u32_e32 v33, vcc, 0, v33, vcc
	v_lshl_add_u64 v[32:33], v[20:21], 0, s[0:1]
	v_readlane_b32 s37, v247, 7
	v_readlane_b32 s38, v247, 8
	v_readlane_b32 s39, v247, 9
	v_readlane_b32 s40, v247, 10
	v_readlane_b32 s41, v247, 11
	v_readlane_b32 s42, v247, 12
	v_readlane_b32 s43, v247, 13
	v_readlane_b32 s44, v247, 14
	v_readlane_b32 s45, v247, 15
	v_readlane_b32 s46, v247, 16
	v_readlane_b32 s47, v247, 17
	v_readlane_b32 s48, v247, 18
	v_readlane_b32 s49, v247, 19
	s_waitcnt lgkmcnt(0)
	ds_read2_b32 v[24:25], v64 offset1:16
	ds_read2_b32 v[26:27], v64 offset0:33 offset1:49
	ds_read2_b32 v[28:29], v64 offset0:66 offset1:82
	ds_read2_b32 v[30:31], v64 offset0:99 offset1:115
	ds_read2_b32 v[36:37], v64 offset0:132 offset1:148
	ds_read2_b32 v[38:39], v64 offset0:165 offset1:181
	ds_read2_b32 v[40:41], v64 offset0:198 offset1:214
	ds_read2_b32 v[42:43], v64 offset0:231 offset1:247
	ds_read2_b32 v[44:45], v85 offset0:8 offset1:24
	ds_read2_b32 v[46:47], v85 offset0:41 offset1:57
	ds_read2_b32 v[48:49], v85 offset0:74 offset1:90
	ds_read2_b32 v[50:51], v85 offset0:107 offset1:123
	s_waitcnt lgkmcnt(11)
	v_mul_f32_e32 v24, 0x43000000, v24
	s_waitcnt lgkmcnt(10)
	v_mul_f32_e32 v26, 0x43000000, v26
	s_waitcnt lgkmcnt(7)
	v_mul_f32_e32 v36, 0x43000000, v36
	s_waitcnt lgkmcnt(6)
	v_mul_f32_e32 v38, 0x43000000, v38
	v_med3_f32 v24, v24, s35, v84
	v_med3_f32 v26, v26, s35, v84
	v_med3_f32 v36, v36, s35, v84
	v_med3_f32 v38, v38, s35, v84
	v_cvt_pk_fp8_f32 v94, v24, v26
	v_cvt_pk_fp8_f32 v95, v36, v38
	v_mul_f32_e32 v28, 0x43000000, v28
	v_mul_f32_e32 v30, 0x43000000, v30
	s_waitcnt lgkmcnt(5)
	v_mul_f32_e32 v40, 0x43000000, v40
	s_waitcnt lgkmcnt(4)
	v_mul_f32_e32 v42, 0x43000000, v42
	s_waitcnt lgkmcnt(3)
	v_mul_f32_e32 v44, 0x43000000, v44
	s_waitcnt lgkmcnt(2)
	v_mul_f32_e32 v46, 0x43000000, v46
	v_med3_f32 v28, v28, s35, v84
	v_med3_f32 v30, v30, s35, v84
	v_med3_f32 v24, v40, s35, v84
	v_med3_f32 v26, v42, s35, v84
	v_cvt_pk_fp8_f32 v94, v28, v30 op_sel:[0,0,1]
	v_cvt_pk_fp8_f32 v95, v24, v26 op_sel:[0,0,1]
	v_med3_f32 v26, v44, s35, v84
	v_med3_f32 v28, v46, s35, v84
	v_cvt_pk_fp8_f32 v96, v26, v28
	ds_read2_b32 v[52:53], v85 offset0:140 offset1:156
	ds_read2_b32 v[54:55], v85 offset0:173 offset1:189
	ds_read2_b32 v[56:57], v85 offset0:206 offset1:222
	s_waitcnt lgkmcnt(4)
	v_mul_f32_e32 v48, 0x43000000, v48
	s_waitcnt lgkmcnt(3)
	v_mul_f32_e32 v24, 0x43000000, v50
	v_med3_f32 v26, v48, s35, v84
	v_med3_f32 v24, v24, s35, v84
	ds_read2_b32 v[58:59], v85 offset0:239 offset1:255
	v_cvt_pk_fp8_f32 v96, v26, v24 op_sel:[0,0,1]
	s_waitcnt lgkmcnt(3)
	v_mul_f32_e32 v24, 0x43000000, v52
	s_waitcnt lgkmcnt(2)
	v_mul_f32_e32 v26, 0x43000000, v54
	v_med3_f32 v24, v24, s35, v84
	v_med3_f32 v26, v26, s35, v84
	v_cvt_pk_fp8_f32 v97, v24, v26
	s_waitcnt lgkmcnt(1)
	v_mul_f32_e32 v28, 0x43000000, v56
	s_waitcnt lgkmcnt(0)
	v_mul_f32_e32 v24, 0x43000000, v58
	v_med3_f32 v26, v28, s35, v84
	v_med3_f32 v24, v24, s35, v84
	v_cvt_pk_fp8_f32 v97, v26, v24 op_sel:[0,0,1]
	v_or_b32_e32 v24, s7, v63
	v_mul_u32_u24_e32 v60, 0x2b00, v24
	v_mul_f32_e32 v24, 0x43000000, v25
	v_mul_f32_e32 v25, 0x43000000, v27
	v_med3_f32 v27, v24, s35, v84
	v_med3_f32 v25, v25, s35, v84
	v_mov_b32_e32 v24, v3
	v_cvt_pk_fp8_f32 v24, v27, v25
	v_mul_f32_e32 v26, 0x43000000, v29
	v_mul_f32_e32 v25, 0x43000000, v31
	v_med3_f32 v26, v26, s35, v84
	v_med3_f32 v25, v25, s35, v84
	v_cvt_pk_fp8_f32 v24, v26, v25 op_sel:[0,0,1]
	v_mul_f32_e32 v25, 0x43000000, v37
	v_mul_f32_e32 v26, 0x43000000, v39
	v_med3_f32 v28, v25, s35, v84
	v_med3_f32 v26, v26, s35, v84
	v_mov_b32_e32 v25, v3
	v_cvt_pk_fp8_f32 v25, v28, v26
	v_mul_f32_e32 v27, 0x43000000, v41
	v_mul_f32_e32 v26, 0x43000000, v43
	v_med3_f32 v27, v27, s35, v84
	v_med3_f32 v26, v26, s35, v84
	v_cvt_pk_fp8_f32 v25, v27, v26 op_sel:[0,0,1]
	v_mul_f32_e32 v26, 0x43000000, v45
	v_mul_f32_e32 v27, 0x43000000, v47
	v_med3_f32 v29, v26, s35, v84
	v_med3_f32 v27, v27, s35, v84
	v_mov_b32_e32 v26, v3
	v_cvt_pk_fp8_f32 v26, v29, v27
	v_mul_f32_e32 v28, 0x43000000, v49
	v_mul_f32_e32 v27, 0x43000000, v51
	v_med3_f32 v28, v28, s35, v84
	v_med3_f32 v27, v27, s35, v84
	v_cvt_pk_fp8_f32 v26, v28, v27 op_sel:[0,0,1]
	v_mul_f32_e32 v27, 0x43000000, v53
	v_mul_f32_e32 v28, 0x43000000, v55
	v_med3_f32 v30, v27, s35, v84
	v_med3_f32 v28, v28, s35, v84
	v_mov_b32_e32 v27, v3
	v_cvt_pk_fp8_f32 v27, v30, v28
	v_mul_f32_e32 v29, 0x43000000, v57
	v_mul_f32_e32 v28, 0x43000000, v59
	v_med3_f32 v29, v29, s35, v84
	v_med3_f32 v28, v28, s35, v84
	v_cvt_pk_fp8_f32 v27, v29, v28 op_sel:[0,0,1]
	v_or_b32_e32 v28, s7, v65
	v_mul_u32_u24_e32 v28, 0x2b00, v28
	v_mov_b32_e32 v29, v3
	v_lshl_add_u64 v[60:61], v[32:33], 0, v[60:61]
	v_lshl_add_u64 v[28:29], v[32:33], 0, v[28:29]
	global_store_dwordx4 v[60:61], v[94:97], off
	global_store_dwordx4 v[28:29], v[24:27], off
	s_waitcnt lgkmcnt(0)

.LBB0_131:
	s_andn2_b64 vcc, exec, s[0:1]
	s_cbranch_vccnz .LBB0_133
	s_add_i32 s0, s3, 0xaa00
	s_and_b32 s1, s0, 0xffff
	s_mul_i32 s1, s1, 0xbe83
	s_lshr_b32 s1, s1, 24
	s_mul_i32 s7, s1, 0x158
	s_sub_i32 s0, s0, s7
	s_lshl_b32 s10, s1, 6
	v_mov_b32_e32 v24, s0
	v_pk_lshlrev_b16 v60, s52, v24 op_sel_hi:[1,0]
	v_or_b32_e32 v24, s10, v35
	v_mul_u32_u24_e32 v24, 0x2b00, v24
	v_readlane_b32 s36, v247, 6
	v_and_b32_e32 v61, 0x7fe0, v60
	v_lshlrev_b32_e32 v24, 2, v24
	v_mov_b32_e32 v25, v3
	v_readlane_b32 s48, v247, 18
	v_readlane_b32 s49, v247, 19
	v_lshlrev_b32_e32 v26, 2, v61
	v_mov_b32_e32 v27, v3
	v_lshl_add_u64 v[24:25], s[48:49], 0, v[24:25]
	v_lshl_add_u64 v[24:25], v[24:25], 0, v[26:27]
	v_lshl_add_u64 v[32:33], v[24:25], 0, v[2:3]
	v_add_co_u32_e32 v28, vcc, s53, v32
	v_readfirstlane_b32 s0, v60
	s_nop 0
	v_addc_co_u32_e32 v29, vcc, 0, v33, vcc
	v_add_co_u32_e32 v36, vcc, s54, v32
	s_nop 0
	v_addc_co_u32_e32 v37, vcc, 0, v33, vcc
	v_add_co_u32_e32 v40, vcc, s55, v32
	s_and_b32 s0, s0, 0x7f000060
	s_nop 0
	v_addc_co_u32_e32 v41, vcc, 0, v33, vcc
	v_add_co_u32_e32 v44, vcc, s56, v32
	s_nop 0
	v_addc_co_u32_e32 v45, vcc, 0, v33, vcc
	v_add_co_u32_e32 v48, vcc, s57, v32
	s_lshr_b32 s1, s0, 16
	s_nop 0
	v_addc_co_u32_e32 v49, vcc, 0, v33, vcc
	s_nop 0
	v_add_co_u32_e32 v52, vcc, s58, v32
	s_or_b32 s0, s0, s1
	s_nop 0
	v_addc_co_u32_e32 v53, vcc, 0, v33, vcc
	v_add_co_u32_e32 v32, vcc, s59, v32
	s_bitset1_b32 s0, 7
	s_nop 0
	v_addc_co_u32_e32 v33, vcc, 0, v33, vcc
	v_or_b32_e32 v32, v63, v61
	v_lshlrev_b32_e32 v32, 2, v32
	s_and_b32 s0, s0, 0xffff
	v_readlane_b32 s37, v247, 7
	v_readlane_b32 s38, v247, 8
	v_readlane_b32 s39, v247, 9
	v_readlane_b32 s40, v247, 10
	v_readlane_b32 s41, v247, 11
	v_readlane_b32 s42, v247, 12
	v_readlane_b32 s43, v247, 13
	v_readlane_b32 s44, v247, 14
	v_readlane_b32 s45, v247, 15
	v_readlane_b32 s46, v247, 16
	v_readlane_b32 s47, v247, 17
	v_readlane_b32 s50, v247, 20
	v_readlane_b32 s51, v247, 21
	s_waitcnt lgkmcnt(0)
	v_mov_b32_e32 v26, v234
	v_or_b32_e32 v27, v65, v61
	v_lshlrev_b32_e32 v27, 2, v27
	ds_read2_b32 v[32:33], v64 offset1:16
	ds_read2_b32 v[36:37], v64 offset0:33 offset1:49
	ds_read2_b32 v[38:39], v64 offset0:66 offset1:82
	ds_read2_b32 v[40:41], v64 offset0:99 offset1:115
	ds_read2_b32 v[42:43], v64 offset0:132 offset1:148
	ds_read2_b32 v[44:45], v64 offset0:165 offset1:181
	ds_read2_b32 v[46:47], v64 offset0:198 offset1:214
	ds_read2_b32 v[48:49], v64 offset0:231 offset1:247
	ds_read2_b32 v[50:51], v85 offset0:8 offset1:24
	ds_read2_b32 v[52:53], v85 offset0:41 offset1:57
	ds_read2_b32 v[54:55], v85 offset0:74 offset1:90
	ds_read2_b32 v[56:57], v85 offset0:107 offset1:123
	ds_read2_b32 v[58:59], v85 offset0:140 offset1:156
	ds_read2_b32 v[60:61], v85 offset0:173 offset1:189
	ds_read2_b32 v[88:89], v85 offset0:206 offset1:222
	v_mov_b32_e32 v87, v235
	v_or_b32_e32 v28, s0, v63
	v_lshlrev_b32_e32 v30, 12, v28
	ds_read2_b32 v[94:95], v85 offset0:239 offset1:255
	v_lshl_add_u64 v[24:25], v[22:23], 0, s[10:11]
	v_div_scale_f32 v27, s[12:13], v26, v26, s61
	v_rcp_f32_e32 v28, v27
	v_div_scale_f32 v29, vcc, s61, v26, s61
	v_fma_f32 v31, -v27, v28, 1.0
	v_fmac_f32_e32 v28, v31, v28
	v_mul_f32_e32 v31, v29, v28
	v_fma_f32 v91, -v27, v31, v29
	v_fmac_f32_e32 v31, v91, v28
	v_fma_f32 v27, -v27, v31, v29
	v_div_fmas_f32 v27, v27, v28, v31
	v_div_fixup_f32 v27, v27, v26, s61
	v_cmp_lt_f32_e32 vcc, 0, v26
	s_nop 1
	v_cndmask_b32_e32 v26, 0, v27, vcc
	s_waitcnt lgkmcnt(14)
	v_mul_f32_e32 v28, v36, v26
	s_waitcnt lgkmcnt(13)
	v_mul_f32_e32 v29, v26, v38
	s_waitcnt lgkmcnt(10)
	v_mul_f32_e32 v36, v26, v44
	s_waitcnt lgkmcnt(9)
	v_mul_f32_e32 v38, v26, v46
	s_waitcnt lgkmcnt(6)
	v_mul_f32_e32 v44, v26, v52
	s_waitcnt lgkmcnt(5)
	v_mul_f32_e32 v46, v26, v54
	s_waitcnt lgkmcnt(2)
	v_mul_f32_e32 v52, v26, v60
	v_mul_f32_e32 v27, v32, v26
	v_mul_f32_e32 v32, v26, v42
	v_mul_f32_e32 v42, v26, v50
	v_mul_f32_e32 v50, v26, v58
	s_waitcnt lgkmcnt(1)
	v_mul_f32_e32 v54, v26, v88
	v_med3_f32 v28, v28, s62, v86
	v_med3_f32 v29, v29, s62, v86
	v_med3_f32 v36, v36, s62, v86
	v_med3_f32 v38, v38, s62, v86
	v_med3_f32 v44, v44, s62, v86
	v_med3_f32 v46, v46, s62, v86
	v_med3_f32 v52, v52, s62, v86
	v_mul_f32_e32 v31, v26, v40
	v_mul_f32_e32 v40, v26, v48
	v_mul_f32_e32 v48, v26, v56
	s_waitcnt lgkmcnt(0)
	v_mul_f32_e32 v26, v26, v94
	v_med3_f32 v27, v27, s62, v86
	v_med3_f32 v32, v32, s62, v86
	v_med3_f32 v42, v42, s62, v86
	v_med3_f32 v50, v50, s62, v86
	v_med3_f32 v54, v54, s62, v86
	v_rndne_f32_e32 v28, v28
	v_rndne_f32_e32 v29, v29
	v_rndne_f32_e32 v36, v36
	v_rndne_f32_e32 v38, v38
	v_rndne_f32_e32 v44, v44
	v_rndne_f32_e32 v46, v46
	v_rndne_f32_e32 v52, v52
	v_med3_f32 v31, v31, s62, v86
	v_med3_f32 v48, v48, s62, v86
	v_med3_f32 v26, v26, s62, v86
	v_rndne_f32_e32 v27, v27
	v_rndne_f32_e32 v32, v32
	v_rndne_f32_e32 v42, v42
	v_rndne_f32_e32 v50, v50
	v_rndne_f32_e32 v54, v54
	v_cvt_i32_f32_e32 v28, v28
	v_cvt_i32_f32_sdwa v29, v29 dst_sel:WORD_1 dst_unused:UNUSED_PAD src0_sel:DWORD
	v_cvt_i32_f32_e32 v36, v36
	v_cvt_i32_f32_sdwa v38, v38 dst_sel:WORD_1 dst_unused:UNUSED_PAD src0_sel:DWORD
	v_cvt_i32_f32_e32 v44, v44
	v_cvt_i32_f32_sdwa v46, v46 dst_sel:WORD_1 dst_unused:UNUSED_PAD src0_sel:DWORD
	v_cvt_i32_f32_e32 v52, v52
	v_med3_f32 v40, v40, s62, v86
	v_rndne_f32_e32 v31, v31
	v_rndne_f32_e32 v48, v48
	v_rndne_f32_e32 v26, v26
	v_cvt_i32_f32_e32 v27, v27
	v_cvt_i32_f32_e32 v32, v32
	v_cvt_i32_f32_e32 v42, v42
	v_cvt_i32_f32_e32 v50, v50
	v_cvt_i32_f32_sdwa v54, v54 dst_sel:WORD_1 dst_unused:UNUSED_PAD src0_sel:DWORD
	v_rndne_f32_e32 v40, v40
	v_cvt_i32_f32_sdwa v31, v31 dst_sel:BYTE_3 dst_unused:UNUSED_PAD src0_sel:DWORD
	v_cvt_i32_f32_sdwa v48, v48 dst_sel:BYTE_3 dst_unused:UNUSED_PAD src0_sel:DWORD
	v_cvt_i32_f32_sdwa v56, v26 dst_sel:BYTE_3 dst_unused:UNUSED_PAD src0_sel:DWORD
	v_cvt_i32_f32_sdwa v40, v40 dst_sel:BYTE_3 dst_unused:UNUSED_PAD src0_sel:DWORD
	v_lshlrev_b32_e32 v26, 8, v28
	v_and_b32_e32 v28, 0xff0000, v29
	v_lshlrev_b32_e32 v29, 8, v36
	v_and_b32_e32 v36, 0xff0000, v38
	v_lshlrev_b32_e32 v38, 8, v44
	v_and_b32_e32 v44, 0xff0000, v46
	v_lshlrev_b32_e32 v46, 8, v52
	v_and_b32_e32 v52, 0xff0000, v54
	v_perm_b32 v26, v26, v27, s63
	v_perm_b32 v27, v29, v32, s63
	v_perm_b32 v29, v38, v42, s63
	v_perm_b32 v32, v46, v50, s63
	v_or3_b32 v26, v26, v28, v31
	v_or3_b32 v28, v29, v44, v48
	v_or3_b32 v29, v32, v52, v56
	v_div_scale_f32 v32, s[12:13], v87, v87, s61
	v_or3_b32 v27, v27, v36, v40
	v_rcp_f32_e32 v36, v32
	v_mov_b32_e32 v31, v3
	v_lshl_add_u64 v[30:31], v[24:25], 0, v[30:31]
	global_store_dwordx4 v[30:31], v[26:29], off
	s_nop 1
	v_fma_f32 v26, -v32, v36, 1.0
	v_fmac_f32_e32 v36, v26, v36
	v_div_scale_f32 v26, vcc, s61, v87, s61
	v_mul_f32_e32 v27, v26, v36
	v_fma_f32 v28, -v32, v27, v26
	v_fmac_f32_e32 v27, v28, v36
	v_fma_f32 v26, -v32, v27, v26
	v_div_fmas_f32 v26, v26, v36, v27
	v_div_fixup_f32 v26, v26, v87, s61
	v_cmp_lt_f32_e32 vcc, 0, v87
	s_nop 1
	v_cndmask_b32_e32 v29, 0, v26, vcc
	v_mul_f32_e32 v27, v37, v29
	v_mul_f32_e32 v26, v33, v29
	v_mul_f32_e32 v28, v29, v39
	v_med3_f32 v27, v27, s62, v86
	v_mul_f32_e32 v30, v29, v41
	v_med3_f32 v26, v26, s62, v86
	v_rndne_f32_e32 v27, v27
	v_med3_f32 v28, v28, s62, v86
	v_rndne_f32_e32 v26, v26
	v_cvt_i32_f32_e32 v27, v27
	v_rndne_f32_e32 v28, v28
	v_med3_f32 v30, v30, s62, v86
	v_cvt_i32_f32_e32 v26, v26
	v_cvt_i32_f32_sdwa v28, v28 dst_sel:WORD_1 dst_unused:UNUSED_PAD src0_sel:DWORD
	v_rndne_f32_e32 v30, v30
	v_cvt_i32_f32_sdwa v30, v30 dst_sel:BYTE_3 dst_unused:UNUSED_PAD src0_sel:DWORD
	v_lshlrev_b32_e32 v27, 8, v27
	v_perm_b32 v26, v27, v26, s63
	v_and_b32_e32 v27, 0xff0000, v28
	v_mul_f32_e32 v28, v29, v45
	v_or3_b32 v26, v26, v27, v30
	v_mul_f32_e32 v27, v29, v43
	v_mul_f32_e32 v30, v29, v47
	v_med3_f32 v28, v28, s62, v86
	v_mul_f32_e32 v31, v29, v49
	v_med3_f32 v27, v27, s62, v86
	v_rndne_f32_e32 v28, v28
	v_med3_f32 v30, v30, s62, v86
	v_rndne_f32_e32 v27, v27
	v_cvt_i32_f32_e32 v28, v28
	v_rndne_f32_e32 v30, v30
	v_med3_f32 v31, v31, s62, v86
	v_cvt_i32_f32_e32 v27, v27
	v_cvt_i32_f32_sdwa v30, v30 dst_sel:WORD_1 dst_unused:UNUSED_PAD src0_sel:DWORD
	v_rndne_f32_e32 v31, v31
	v_cvt_i32_f32_sdwa v31, v31 dst_sel:BYTE_3 dst_unused:UNUSED_PAD src0_sel:DWORD
	v_lshlrev_b32_e32 v28, 8, v28
	v_perm_b32 v27, v28, v27, s63
	v_and_b32_e32 v28, 0xff0000, v30
	v_mul_f32_e32 v30, v29, v53
	v_or3_b32 v27, v27, v28, v31
	v_mul_f32_e32 v28, v29, v51
	v_mul_f32_e32 v31, v29, v55
	v_med3_f32 v30, v30, s62, v86
	v_mul_f32_e32 v32, v29, v57
	v_med3_f32 v28, v28, s62, v86
	v_rndne_f32_e32 v30, v30
	v_med3_f32 v31, v31, s62, v86
	v_rndne_f32_e32 v28, v28
	v_cvt_i32_f32_e32 v30, v30
	v_rndne_f32_e32 v31, v31
	v_med3_f32 v32, v32, s62, v86
	v_cvt_i32_f32_e32 v28, v28
	v_cvt_i32_f32_sdwa v31, v31 dst_sel:WORD_1 dst_unused:UNUSED_PAD src0_sel:DWORD
	v_rndne_f32_e32 v32, v32
	v_cvt_i32_f32_sdwa v32, v32 dst_sel:BYTE_3 dst_unused:UNUSED_PAD src0_sel:DWORD
	v_lshlrev_b32_e32 v30, 8, v30
	v_perm_b32 v28, v30, v28, s63
	v_and_b32_e32 v30, 0xff0000, v31
	v_mul_f32_e32 v31, v29, v61
	v_or3_b32 v28, v28, v30, v32
	v_mul_f32_e32 v30, v29, v59
	v_mul_f32_e32 v32, v29, v89
	v_med3_f32 v31, v31, s62, v86
	v_mul_f32_e32 v29, v29, v95
	v_med3_f32 v30, v30, s62, v86
	v_rndne_f32_e32 v31, v31
	v_med3_f32 v32, v32, s62, v86
	v_rndne_f32_e32 v30, v30
	v_cvt_i32_f32_e32 v31, v31
	v_rndne_f32_e32 v32, v32
	v_med3_f32 v29, v29, s62, v86
	v_cvt_i32_f32_e32 v30, v30
	v_cvt_i32_f32_sdwa v32, v32 dst_sel:WORD_1 dst_unused:UNUSED_PAD src0_sel:DWORD
	v_rndne_f32_e32 v29, v29
	v_cvt_i32_f32_sdwa v29, v29 dst_sel:BYTE_3 dst_unused:UNUSED_PAD src0_sel:DWORD
	v_lshlrev_b32_e32 v31, 8, v31
	v_perm_b32 v30, v31, v30, s63
	v_and_b32_e32 v31, 0xff0000, v32
	v_or3_b32 v29, v30, v31, v29
	v_or_b32_e32 v30, s0, v65
	v_lshlrev_b32_e32 v30, 12, v30
	v_mov_b32_e32 v31, v3
	v_lshl_add_u64 v[24:25], v[24:25], 0, v[30:31]
	global_store_dwordx4 v[24:25], v[26:29], off
	s_waitcnt lgkmcnt(0)

.LBB0_134:
	s_andn2_b64 vcc, exec, s[0:1]
	s_cbranch_vccnz .LBB0_87
	s_mul_hi_i32 s0, s3, 0x2fa0be83
	s_lshr_b32 s1, s0, 31
	s_ashr_i32 s0, s0, 6
	s_add_i32 s0, s0, s1
	v_readlane_b32 s36, v247, 6
	s_lshl_b32 s12, s0, 6
	s_mulk_i32 s0, 0xd500
	v_readlane_b32 s46, v247, 16
	v_readlane_b32 s47, v247, 17
	s_add_i32 s0, s14, s0
	v_or_b32_e32 v26, s12, v35
	v_mov_b64_e32 v[24:25], s[46:47]
	s_mov_b32 s1, 0xac00
	v_mad_i64_i32 v[24:25], s[24:25], v26, s1, v[24:25]
	s_ashr_i32 s1, s0, 31
	v_lshl_add_u64 v[24:25], s[0:1], 2, v[24:25]
	v_lshl_add_u64 v[24:25], v[24:25], 0, v[2:3]
	v_add_co_u32_e32 v26, vcc, s53, v24
	s_ashr_i32 s13, s12, 31
	s_nop 0
	v_addc_co_u32_e32 v27, vcc, 0, v25, vcc
	v_add_co_u32_e32 v26, vcc, s54, v24
	s_bfe_u32 s1, s0, 0x70018
	s_nop 0
	v_addc_co_u32_e32 v27, vcc, 0, v25, vcc
	v_add_co_u32_e32 v32, vcc, s55, v24
	s_add_i32 s1, s0, s1
	s_nop 0
	v_addc_co_u32_e32 v33, vcc, 0, v25, vcc
	v_add_co_u32_e32 v26, vcc, s56, v24
	s_sext_i32_i16 s7, s1
	s_nop 0
	v_addc_co_u32_e32 v27, vcc, 0, v25, vcc
	v_add_co_u32_e32 v32, vcc, s57, v24
	s_and_b32 s1, s1, 0xff80
	s_nop 0
	v_addc_co_u32_e32 v33, vcc, 0, v25, vcc
	v_add_co_u32_e32 v26, vcc, s58, v24
	s_lshl_b32 s7, s7, 1
	s_nop 0
	v_addc_co_u32_e32 v27, vcc, 0, v25, vcc
	v_add_co_u32_e32 v24, vcc, s59, v24
	v_readlane_b32 s37, v247, 7
	s_nop 0
	v_addc_co_u32_e32 v25, vcc, 0, v25, vcc
	v_add_u32_e32 v26, s0, v63
	v_ashrrev_i32_e32 v27, 31, v26
	v_lshl_add_u64 v[24:25], v[26:27], 2, s[28:29]
	s_sub_i32 s0, s0, s1
	s_and_b32 s1, s7, 0xffffff00
	s_sext_i32_i16 s0, s0
	s_add_i32 s0, s1, s0
	v_or_b32_e32 v88, s0, v63
	v_ashrrev_i32_e32 v89, 31, v88
	v_lshlrev_b64 v[88:89], 12, v[88:89]
	v_add_u32_e32 v26, 16, v26
	v_readlane_b32 s38, v247, 8
	v_readlane_b32 s39, v247, 9
	v_readlane_b32 s40, v247, 10
	v_readlane_b32 s41, v247, 11
	v_readlane_b32 s42, v247, 12
	v_readlane_b32 s43, v247, 13
	v_readlane_b32 s44, v247, 14
	v_readlane_b32 s45, v247, 15
	v_readlane_b32 s48, v247, 18
	v_readlane_b32 s49, v247, 19
	v_readlane_b32 s50, v247, 20
	v_readlane_b32 s51, v247, 21
	s_waitcnt lgkmcnt(0)
	v_mov_b32_e32 v27, v234
	v_lshl_add_u64 v[24:25], v[22:23], 0, s[12:13]
	ds_read2_b32 v[28:29], v64 offset1:16
	ds_read2_b32 v[30:31], v64 offset0:33 offset1:49
	ds_read2_b32 v[32:33], v64 offset0:66 offset1:82
	ds_read2_b32 v[36:37], v64 offset0:99 offset1:115
	ds_read2_b32 v[38:39], v64 offset0:132 offset1:148
	ds_read2_b32 v[40:41], v64 offset0:165 offset1:181
	ds_read2_b32 v[42:43], v64 offset0:198 offset1:214
	ds_read2_b32 v[44:45], v64 offset0:231 offset1:247
	ds_read2_b32 v[46:47], v85 offset0:8 offset1:24
	ds_read2_b32 v[48:49], v85 offset0:41 offset1:57
	ds_read2_b32 v[50:51], v85 offset0:74 offset1:90
	ds_read2_b32 v[52:53], v85 offset0:107 offset1:123
	ds_read2_b32 v[54:55], v85 offset0:140 offset1:156
	ds_read2_b32 v[56:57], v85 offset0:173 offset1:189
	ds_read2_b32 v[58:59], v85 offset0:206 offset1:222
	ds_read2_b32 v[60:61], v85 offset0:239 offset1:255
	v_lshl_add_u64 v[88:89], v[24:25], 0, v[88:89]
	v_div_scale_f32 v87, s[12:13], v27, v27, s61
	v_rcp_f32_e32 v91, v87
	v_div_scale_f32 v93, vcc, s61, v27, s61
	v_fma_f32 v94, -v87, v91, 1.0
	v_fmac_f32_e32 v91, v94, v91
	v_mul_f32_e32 v94, v93, v91
	v_fma_f32 v95, -v87, v94, v93
	v_fmac_f32_e32 v94, v95, v91
	v_fma_f32 v87, -v87, v94, v93
	v_div_fmas_f32 v87, v87, v91, v94
	v_div_fixup_f32 v87, v87, v27, s61
	v_cmp_lt_f32_e32 vcc, 0, v27
	s_nop 1
	v_cndmask_b32_e32 v27, 0, v87, vcc
	s_waitcnt lgkmcnt(14)
	v_mul_f32_e32 v30, v30, v27
	s_waitcnt lgkmcnt(10)
	v_mul_f32_e32 v40, v27, v40
	s_waitcnt lgkmcnt(6)
	v_mul_f32_e32 v48, v27, v48
	s_waitcnt lgkmcnt(2)
	v_mul_f32_e32 v56, v27, v56
	v_mul_f32_e32 v28, v28, v27
	v_mul_f32_e32 v32, v27, v32
	v_mul_f32_e32 v38, v27, v38
	v_mul_f32_e32 v42, v27, v42
	v_mul_f32_e32 v46, v27, v46
	v_mul_f32_e32 v50, v27, v50
	v_mul_f32_e32 v54, v27, v54
	s_waitcnt lgkmcnt(1)
	v_mul_f32_e32 v58, v27, v58
	v_med3_f32 v30, v30, s62, v86
	v_med3_f32 v40, v40, s62, v86
	v_med3_f32 v48, v48, s62, v86
	v_med3_f32 v56, v56, s62, v86
	v_mul_f32_e32 v36, v27, v36
	v_mul_f32_e32 v44, v27, v44
	v_mul_f32_e32 v52, v27, v52
	s_waitcnt lgkmcnt(0)
	v_mul_f32_e32 v27, v27, v60
	v_med3_f32 v28, v28, s62, v86
	v_med3_f32 v32, v32, s62, v86
	v_med3_f32 v38, v38, s62, v86
	v_med3_f32 v42, v42, s62, v86
	v_med3_f32 v46, v46, s62, v86
	v_med3_f32 v50, v50, s62, v86
	v_med3_f32 v54, v54, s62, v86
	v_med3_f32 v58, v58, s62, v86
	v_rndne_f32_e32 v30, v30
	v_rndne_f32_e32 v40, v40
	v_rndne_f32_e32 v48, v48
	v_rndne_f32_e32 v56, v56
	v_med3_f32 v36, v36, s62, v86
	v_med3_f32 v44, v44, s62, v86
	v_med3_f32 v52, v52, s62, v86
	v_med3_f32 v27, v27, s62, v86
	v_rndne_f32_e32 v28, v28
	v_rndne_f32_e32 v32, v32
	v_rndne_f32_e32 v38, v38
	v_rndne_f32_e32 v42, v42
	v_rndne_f32_e32 v46, v46
	v_rndne_f32_e32 v50, v50
	v_rndne_f32_e32 v54, v54
	v_rndne_f32_e32 v58, v58
	v_cvt_i32_f32_e32 v30, v30
	v_cvt_i32_f32_e32 v40, v40
	v_cvt_i32_f32_e32 v48, v48
	v_cvt_i32_f32_e32 v56, v56
	v_rndne_f32_e32 v36, v36
	v_rndne_f32_e32 v44, v44
	v_rndne_f32_e32 v52, v52
	v_rndne_f32_e32 v27, v27
	v_cvt_i32_f32_e32 v28, v28
	v_cvt_i32_f32_sdwa v32, v32 dst_sel:WORD_1 dst_unused:UNUSED_PAD src0_sel:DWORD
	v_cvt_i32_f32_e32 v38, v38
	v_cvt_i32_f32_sdwa v42, v42 dst_sel:WORD_1 dst_unused:UNUSED_PAD src0_sel:DWORD
	v_cvt_i32_f32_e32 v46, v46
	v_cvt_i32_f32_sdwa v50, v50 dst_sel:WORD_1 dst_unused:UNUSED_PAD src0_sel:DWORD
	v_cvt_i32_f32_e32 v54, v54
	v_cvt_i32_f32_sdwa v58, v58 dst_sel:WORD_1 dst_unused:UNUSED_PAD src0_sel:DWORD
	v_cvt_i32_f32_sdwa v36, v36 dst_sel:BYTE_3 dst_unused:UNUSED_PAD src0_sel:DWORD
	v_cvt_i32_f32_sdwa v44, v44 dst_sel:BYTE_3 dst_unused:UNUSED_PAD src0_sel:DWORD
	v_cvt_i32_f32_sdwa v52, v52 dst_sel:BYTE_3 dst_unused:UNUSED_PAD src0_sel:DWORD
	v_cvt_i32_f32_sdwa v27, v27 dst_sel:BYTE_3 dst_unused:UNUSED_PAD src0_sel:DWORD
	v_lshlrev_b32_e32 v30, 8, v30
	v_lshlrev_b32_e32 v40, 8, v40
	v_lshlrev_b32_e32 v48, 8, v48
	v_lshlrev_b32_e32 v56, 8, v56
	v_and_b32_e32 v32, 0xff0000, v32
	v_and_b32_e32 v42, 0xff0000, v42
	v_and_b32_e32 v50, 0xff0000, v50
	v_and_b32_e32 v58, 0xff0000, v58
	v_perm_b32 v28, v30, v28, s63
	v_perm_b32 v30, v40, v38, s63
	v_perm_b32 v38, v48, v46, s63
	v_perm_b32 v40, v56, v54, s63
	v_or3_b32 v94, v28, v32, v36
	v_or3_b32 v95, v30, v42, v44
	v_or3_b32 v96, v38, v50, v52
	v_or3_b32 v97, v40, v58, v27
	v_ashrrev_i32_e32 v27, 31, v26
	global_store_dwordx4 v[88:89], v[94:97], off
	v_lshl_add_u64 v[26:27], v[26:27], 2, s[28:29]
	v_mov_b32_e32 v26, v235
	v_or_b32_e32 v88, s0, v65
	v_ashrrev_i32_e32 v89, 31, v88
	v_div_scale_f32 v27, s[0:1], v26, v26, s61
	v_rcp_f32_e32 v28, v27
	v_div_scale_f32 v30, vcc, s61, v26, s61
	v_fma_f32 v32, -v27, v28, 1.0
	v_fmac_f32_e32 v28, v32, v28
	v_mul_f32_e32 v32, v30, v28
	v_fma_f32 v36, -v27, v32, v30
	v_fmac_f32_e32 v32, v36, v28
	v_fma_f32 v27, -v27, v32, v30
	v_div_fmas_f32 v27, v27, v28, v32
	v_div_fixup_f32 v27, v27, v26, s61
	v_cmp_lt_f32_e32 vcc, 0, v26
	s_nop 1
	v_cndmask_b32_e32 v26, 0, v27, vcc
	v_mul_f32_e32 v27, v29, v26
	v_mul_f32_e32 v28, v31, v26
	v_mul_f32_e32 v29, v26, v33
	v_mul_f32_e32 v31, v26, v39
	v_mul_f32_e32 v32, v26, v41
	v_mul_f32_e32 v33, v26, v43
	v_mul_f32_e32 v38, v26, v49
	v_mul_f32_e32 v39, v26, v51
	v_mul_f32_e32 v42, v26, v57
	v_mul_f32_e32 v30, v26, v37
	v_mul_f32_e32 v37, v26, v47
	v_mul_f32_e32 v41, v26, v55
	v_mul_f32_e32 v43, v26, v59
	v_med3_f32 v28, v28, s62, v86
	v_med3_f32 v29, v29, s62, v86
	v_med3_f32 v32, v32, s62, v86
	v_med3_f32 v33, v33, s62, v86
	v_med3_f32 v38, v38, s62, v86
	v_med3_f32 v39, v39, s62, v86
	v_med3_f32 v42, v42, s62, v86
	v_mul_f32_e32 v36, v26, v45
	v_mul_f32_e32 v40, v26, v53
	v_mul_f32_e32 v26, v26, v61
	v_med3_f32 v27, v27, s62, v86
	v_med3_f32 v31, v31, s62, v86
	v_med3_f32 v37, v37, s62, v86
	v_med3_f32 v41, v41, s62, v86
	v_med3_f32 v43, v43, s62, v86
	v_rndne_f32_e32 v28, v28
	v_rndne_f32_e32 v29, v29
	v_rndne_f32_e32 v32, v32
	v_rndne_f32_e32 v33, v33
	v_rndne_f32_e32 v38, v38
	v_rndne_f32_e32 v39, v39
	v_rndne_f32_e32 v42, v42
	v_med3_f32 v30, v30, s62, v86
	v_med3_f32 v40, v40, s62, v86
	v_med3_f32 v26, v26, s62, v86
	v_rndne_f32_e32 v27, v27
	v_rndne_f32_e32 v31, v31
	v_rndne_f32_e32 v37, v37
	v_rndne_f32_e32 v41, v41
	v_rndne_f32_e32 v43, v43
	v_cvt_i32_f32_e32 v28, v28
	v_cvt_i32_f32_sdwa v29, v29 dst_sel:WORD_1 dst_unused:UNUSED_PAD src0_sel:DWORD
	v_cvt_i32_f32_e32 v32, v32
	v_cvt_i32_f32_sdwa v33, v33 dst_sel:WORD_1 dst_unused:UNUSED_PAD src0_sel:DWORD
	v_cvt_i32_f32_e32 v38, v38
	v_cvt_i32_f32_sdwa v39, v39 dst_sel:WORD_1 dst_unused:UNUSED_PAD src0_sel:DWORD
	v_cvt_i32_f32_e32 v42, v42
	v_med3_f32 v36, v36, s62, v86
	v_rndne_f32_e32 v30, v30
	v_rndne_f32_e32 v40, v40
	v_rndne_f32_e32 v26, v26
	v_cvt_i32_f32_e32 v27, v27
	v_cvt_i32_f32_e32 v31, v31
	v_cvt_i32_f32_e32 v37, v37
	v_cvt_i32_f32_e32 v41, v41
	v_cvt_i32_f32_sdwa v43, v43 dst_sel:WORD_1 dst_unused:UNUSED_PAD src0_sel:DWORD
	v_rndne_f32_e32 v36, v36
	v_cvt_i32_f32_sdwa v30, v30 dst_sel:BYTE_3 dst_unused:UNUSED_PAD src0_sel:DWORD
	v_cvt_i32_f32_sdwa v40, v40 dst_sel:BYTE_3 dst_unused:UNUSED_PAD src0_sel:DWORD
	v_cvt_i32_f32_sdwa v44, v26 dst_sel:BYTE_3 dst_unused:UNUSED_PAD src0_sel:DWORD
	v_cvt_i32_f32_sdwa v36, v36 dst_sel:BYTE_3 dst_unused:UNUSED_PAD src0_sel:DWORD
	v_lshlrev_b32_e32 v26, 8, v28
	v_and_b32_e32 v28, 0xff0000, v29
	v_lshlrev_b32_e32 v29, 8, v32
	v_and_b32_e32 v32, 0xff0000, v33
	v_lshlrev_b32_e32 v33, 8, v38
	v_and_b32_e32 v38, 0xff0000, v39
	v_lshlrev_b32_e32 v39, 8, v42
	v_and_b32_e32 v42, 0xff0000, v43
	v_perm_b32 v26, v26, v27, s63
	v_perm_b32 v27, v29, v31, s63
	v_perm_b32 v29, v33, v37, s63
	v_perm_b32 v31, v39, v41, s63
	v_or3_b32 v26, v26, v28, v30
	v_or3_b32 v28, v29, v38, v40
	v_or3_b32 v29, v31, v42, v44
	v_lshlrev_b64 v[30:31], 12, v[88:89]
	v_or3_b32 v27, v27, v32, v36
	v_lshl_add_u64 v[24:25], v[24:25], 0, v[30:31]
	global_store_dwordx4 v[24:25], v[26:29], off
	s_waitcnt lgkmcnt(0)
	s_branch .LBB0_87
